# hoisted the serialized x / x1h row loads in the P7 and P11 norm loops to the loop top (counted vmcnt)
# speedup vs baseline: 1.0038x; 1.0038x over previous
.LBB0_1556:
	v_lshl_add_u64 v[32:33], s[68:69], 0, v[14:15]
	v_add_co_u32_e32 v22, vcc, s9, v32
	s_nop 1
	v_addc_co_u32_e32 v23, vcc, 0, v33, vcc
	global_load_dwordx4 v[2:5], v[22:23], off
	global_load_dwordx4 v[6:9], v[22:23], off offset:1024
	global_load_dwordx4 v[18:21], v[22:23], off offset:2048
	global_load_dwordx4 v[28:31], v[22:23], off offset:3072
	v_add_co_u32_e32 v22, vcc, 0x2fa00000, v32
	s_waitcnt vmcnt(3)
	v_cvt_f32_f16_e32 v72, v4
	v_addc_co_u32_e32 v23, vcc, 0, v33, vcc
	global_load_dwordx4 v[34:37], v[22:23], off
	global_load_dwordx4 v[40:43], v[22:23], off offset:1024
	global_load_dwordx4 v[48:51], v[22:23], off offset:2048
	global_load_dwordx4 v[64:67], v[22:23], off offset:3072
	global_load_dwordx4 v[130:133], v[16:17], off
	global_load_dwordx4 v[134:137], v[16:17], off offset:16
	global_load_dwordx4 v[138:141], v[16:17], off offset:2048
	global_load_dwordx4 v[142:145], v[16:17], off offset:2064
	v_add_co_u32_e32 v216, vcc, s29, v16
	s_nop 1
	v_addc_co_u32_e32 v217, vcc, 0, v17, vcc
	v_add_co_u32_e32 v218, vcc, s31, v16
	s_nop 1
	v_addc_co_u32_e32 v219, vcc, 0, v17, vcc
	global_load_dwordx4 v[146:149], v[216:217], off offset:-4096
	global_load_dwordx4 v[150:153], v[216:217], off offset:-4080
	global_load_dwordx4 v[154:157], v[216:217], off offset:-2048
	global_load_dwordx4 v[158:161], v[216:217], off offset:-2032
	global_load_dwordx4 v[168:171], v[216:217], off
	global_load_dwordx4 v[172:175], v[216:217], off offset:16
	global_load_dwordx4 v[176:179], v[216:217], off offset:2048
	global_load_dwordx4 v[180:183], v[216:217], off offset:2064
	global_load_dwordx4 v[184:187], v[218:219], off
	global_load_dwordx4 v[188:191], v[218:219], off offset:16
	global_load_dwordx4 v[192:195], v[218:219], off offset:2048
	global_load_dwordx4 v[196:199], v[218:219], off offset:2064
	v_cvt_f32_f16_sdwa v73, v4 dst_sel:DWORD dst_unused:UNUSED_PAD src0_sel:WORD_1
	v_cvt_f32_f16_e32 v74, v5
	v_cvt_f32_f16_sdwa v75, v5 dst_sel:DWORD dst_unused:UNUSED_PAD src0_sel:WORD_1
	s_waitcnt vmcnt(22)
	v_cvt_f32_f16_e32 v52, v8
	v_cvt_f32_f16_sdwa v53, v8 dst_sel:DWORD dst_unused:UNUSED_PAD src0_sel:WORD_1
	v_cvt_f32_f16_e32 v54, v9
	v_cvt_f32_f16_sdwa v55, v9 dst_sel:DWORD dst_unused:UNUSED_PAD src0_sel:WORD_1
	s_waitcnt vmcnt(21)
	v_cvt_f32_f16_e32 v8, v19
	v_cvt_f32_f16_sdwa v9, v19 dst_sel:DWORD dst_unused:UNUSED_PAD src0_sel:WORD_1
	v_cvt_f32_f16_e32 v4, v21
	v_cvt_f32_f16_sdwa v5, v21 dst_sel:DWORD dst_unused:UNUSED_PAD src0_sel:WORD_1
	v_cvt_f32_f16_e32 v68, v2
	v_cvt_f32_f16_sdwa v69, v2 dst_sel:DWORD dst_unused:UNUSED_PAD src0_sel:WORD_1
	v_cvt_f32_f16_e32 v70, v3
	v_cvt_f32_f16_sdwa v71, v3 dst_sel:DWORD dst_unused:UNUSED_PAD src0_sel:WORD_1
	v_cvt_f32_f16_e32 v56, v6
	v_cvt_f32_f16_sdwa v57, v6 dst_sel:DWORD dst_unused:UNUSED_PAD src0_sel:WORD_1
	v_cvt_f32_f16_e32 v58, v7
	v_cvt_f32_f16_sdwa v59, v7 dst_sel:DWORD dst_unused:UNUSED_PAD src0_sel:WORD_1
	v_cvt_f32_f16_e32 v6, v18
	v_cvt_f32_f16_sdwa v7, v18 dst_sel:DWORD dst_unused:UNUSED_PAD src0_sel:WORD_1
	v_cvt_f32_f16_e32 v2, v20
	v_cvt_f32_f16_sdwa v3, v20 dst_sel:DWORD dst_unused:UNUSED_PAD src0_sel:WORD_1
	s_waitcnt vmcnt(20)
	v_cvt_f32_f16_e32 v24, v28
	v_cvt_f32_f16_sdwa v25, v28 dst_sel:DWORD dst_unused:UNUSED_PAD src0_sel:WORD_1
	v_cvt_f32_f16_e32 v26, v29
	v_cvt_f32_f16_sdwa v27, v29 dst_sel:DWORD dst_unused:UNUSED_PAD src0_sel:WORD_1
	v_cvt_f32_f16_e32 v28, v30
	v_cvt_f32_f16_sdwa v29, v30 dst_sel:DWORD dst_unused:UNUSED_PAD src0_sel:WORD_1
	v_cvt_f32_f16_e32 v30, v31
	v_cvt_f32_f16_sdwa v31, v31 dst_sel:DWORD dst_unused:UNUSED_PAD src0_sel:WORD_1
	s_waitcnt vmcnt(19)
	v_cvt_f32_f16_sdwa v19, v34 dst_sel:DWORD dst_unused:UNUSED_PAD src0_sel:WORD_1
	v_cvt_f32_f16_sdwa v21, v35 dst_sel:DWORD dst_unused:UNUSED_PAD src0_sel:WORD_1
	v_cvt_f32_f16_e32 v18, v34
	v_cvt_f32_f16_e32 v20, v35
	v_cvt_f32_f16_sdwa v35, v36 dst_sel:DWORD dst_unused:UNUSED_PAD src0_sel:WORD_1
	v_cvt_f32_f16_sdwa v77, v37 dst_sel:DWORD dst_unused:UNUSED_PAD src0_sel:WORD_1
	v_cvt_f32_f16_e32 v34, v36
	v_cvt_f32_f16_e32 v76, v37
	s_waitcnt vmcnt(18)
	v_cvt_f32_f16_e32 v36, v40
	v_cvt_f32_f16_sdwa v37, v40 dst_sel:DWORD dst_unused:UNUSED_PAD src0_sel:WORD_1
	v_cvt_f32_f16_e32 v38, v41
	v_mov_b32_e32 v78, v19
	v_mov_b32_e32 v79, v21
	v_cvt_f32_f16_sdwa v39, v41 dst_sel:DWORD dst_unused:UNUSED_PAD src0_sel:WORD_1
	v_cvt_f32_f16_e32 v40, v42
	v_cvt_f32_f16_sdwa v41, v42 dst_sel:DWORD dst_unused:UNUSED_PAD src0_sel:WORD_1
	v_cvt_f32_f16_e32 v42, v43
	v_cvt_f32_f16_sdwa v43, v43 dst_sel:DWORD dst_unused:UNUSED_PAD src0_sel:WORD_1
	v_mov_b32_e32 v22, v18
	v_mov_b32_e32 v23, v20
	v_pk_mul_f32 v[78:79], v[78:79], v[78:79]
	s_waitcnt vmcnt(17)
	v_cvt_f32_f16_sdwa v45, v48 dst_sel:DWORD dst_unused:UNUSED_PAD src0_sel:WORD_1
	v_pk_fma_f32 v[22:23], v[22:23], v[22:23], v[78:79]
	v_mov_b32_e32 v78, v35
	v_mov_b32_e32 v79, v77
	v_cvt_f32_f16_sdwa v47, v49 dst_sel:DWORD dst_unused:UNUSED_PAD src0_sel:WORD_1
	v_mov_b32_e32 v80, v34
	v_mov_b32_e32 v81, v76
	v_pk_mul_f32 v[78:79], v[78:79], v[78:79]
	v_mul_f32_e32 v10, v36, v36
	v_cvt_f32_f16_e32 v44, v48
	v_cvt_f32_f16_e32 v46, v49
	v_cvt_f32_f16_e32 v48, v50
	v_pk_fma_f32 v[78:79], v[80:81], v[80:81], v[78:79]
	v_pk_fma_f32 v[80:81], v[36:37], v[36:37], v[10:11] op_sel_hi:[1,1,0]
	v_mul_f32_e32 v10, v38, v38
	v_cvt_f32_f16_sdwa v49, v50 dst_sel:DWORD dst_unused:UNUSED_PAD src0_sel:WORD_1
	v_cvt_f32_f16_e32 v50, v51
	v_pk_add_f32 v[22:23], v[22:23], v[22:23] op_sel_hi:[0,1]
	v_pk_add_f32 v[78:79], v[78:79], v[78:79] op_sel_hi:[0,1]
	v_pk_fma_f32 v[82:83], v[38:39], v[38:39], v[10:11] op_sel_hi:[1,1,0]
	v_pk_mul_f32 v[100:101], v[40:41], v[40:41]
	v_pk_mul_f32 v[102:103], v[42:43], v[42:43]
	v_cvt_f32_f16_sdwa v51, v51 dst_sel:DWORD dst_unused:UNUSED_PAD src0_sel:WORD_1
	s_waitcnt vmcnt(16)
	v_cvt_f32_f16_e32 v60, v64
	v_cvt_f32_f16_sdwa v61, v64 dst_sel:DWORD dst_unused:UNUSED_PAD src0_sel:WORD_1
	v_cvt_f32_f16_e32 v62, v65
	v_cvt_f32_f16_sdwa v63, v65 dst_sel:DWORD dst_unused:UNUSED_PAD src0_sel:WORD_1
	v_mov_b32_e32 v22, v100
	v_mov_b32_e32 v78, v101
	v_mov_b32_e32 v80, v102
	v_mov_b32_e32 v82, v103
	v_pk_add_f32 v[22:23], v[22:23], v[78:79]
	v_pk_add_f32 v[78:79], v[80:81], v[82:83]
	v_mov_b32_e32 v80, v45
	v_mov_b32_e32 v81, v47
	v_pk_add_f32 v[22:23], v[22:23], v[78:79]
	v_mov_b32_e32 v78, v44
	v_mov_b32_e32 v79, v46
	v_pk_mul_f32 v[80:81], v[80:81], v[80:81]
	v_mul_f32_e32 v10, v48, v48
	v_cvt_f32_f16_e32 v64, v66
	v_cvt_f32_f16_sdwa v65, v66 dst_sel:DWORD dst_unused:UNUSED_PAD src0_sel:WORD_1
	v_cvt_f32_f16_e32 v66, v67
	v_cvt_f32_f16_sdwa v67, v67 dst_sel:DWORD dst_unused:UNUSED_PAD src0_sel:WORD_1
	v_pk_fma_f32 v[78:79], v[78:79], v[78:79], v[80:81]
	v_pk_fma_f32 v[80:81], v[48:49], v[48:49], v[10:11] op_sel_hi:[1,1,0]
	v_mul_f32_e32 v10, v50, v50
	v_pk_add_f32 v[22:23], v[22:23], v[22:23] op_sel_hi:[0,1]
	v_pk_add_f32 v[78:79], v[78:79], v[78:79] op_sel_hi:[0,1]
	v_pk_fma_f32 v[82:83], v[50:51], v[50:51], v[10:11] op_sel_hi:[1,1,0]
	v_pk_mul_f32 v[100:101], v[60:61], v[60:61]
	v_pk_mul_f32 v[102:103], v[62:63], v[62:63]
	v_mov_b32_e32 v80, v100
	v_mov_b32_e32 v82, v101
	v_mov_b32_e32 v78, v102
	v_mov_b32_e32 v22, v103
	v_pk_add_f32 v[80:81], v[80:81], v[82:83]
	v_pk_add_f32 v[22:23], v[78:79], v[22:23]
	v_mov_b32_e32 v78, v64
	v_pk_add_f32 v[22:23], v[80:81], v[22:23]
	v_mov_b32_e32 v80, v65
	v_mov_b32_e32 v81, v67
	v_mov_b32_e32 v79, v66
	v_pk_mul_f32 v[80:81], v[80:81], v[80:81]
	v_mul_f32_e32 v10, v68, v68
	v_pk_fma_f32 v[78:79], v[78:79], v[78:79], v[80:81]
	v_pk_fma_f32 v[80:81], v[68:69], v[68:69], v[10:11] op_sel_hi:[1,1,0]
	v_mul_f32_e32 v10, v70, v70
	v_pk_add_f32 v[22:23], v[22:23], v[22:23] op_sel_hi:[0,1]
	v_pk_add_f32 v[78:79], v[78:79], v[78:79] op_sel_hi:[0,1]
	v_pk_fma_f32 v[82:83], v[70:71], v[70:71], v[10:11] op_sel_hi:[1,1,0]
	v_pk_mul_f32 v[100:101], v[72:73], v[72:73]
	v_pk_mul_f32 v[102:103], v[74:75], v[74:75]
	v_mov_b32_e32 v80, v100
	v_mov_b32_e32 v82, v101
	v_mov_b32_e32 v78, v102
	v_mov_b32_e32 v22, v103
	v_pk_add_f32 v[80:81], v[80:81], v[82:83]
	v_pk_add_f32 v[22:23], v[78:79], v[22:23]
	v_mov_b32_e32 v78, v56
	v_pk_add_f32 v[22:23], v[80:81], v[22:23]
	v_mov_b32_e32 v80, v57
	v_mov_b32_e32 v81, v59
	v_mov_b32_e32 v79, v58
	v_pk_mul_f32 v[80:81], v[80:81], v[80:81]
	v_mul_f32_e32 v10, v52, v52
	v_pk_fma_f32 v[78:79], v[78:79], v[78:79], v[80:81]
	v_pk_fma_f32 v[80:81], v[52:53], v[52:53], v[10:11] op_sel_hi:[1,1,0]
	v_mul_f32_e32 v10, v54, v54
	v_pk_add_f32 v[22:23], v[22:23], v[22:23] op_sel_hi:[0,1]
	v_pk_add_f32 v[78:79], v[78:79], v[78:79] op_sel_hi:[0,1]
	v_pk_fma_f32 v[82:83], v[54:55], v[54:55], v[10:11] op_sel_hi:[1,1,0]
	v_pk_mul_f32 v[100:101], v[6:7], v[6:7]
	v_pk_mul_f32 v[102:103], v[8:9], v[8:9]
	v_mov_b32_e32 v80, v100
	v_mov_b32_e32 v82, v101
	v_mov_b32_e32 v78, v102
	v_mov_b32_e32 v22, v103
	v_pk_add_f32 v[80:81], v[80:81], v[82:83]
	v_pk_add_f32 v[22:23], v[78:79], v[22:23]
	v_mov_b32_e32 v78, v2
	v_pk_add_f32 v[22:23], v[80:81], v[22:23]
	v_mov_b32_e32 v80, v3
	v_mov_b32_e32 v81, v5
	v_mov_b32_e32 v79, v4
	v_pk_mul_f32 v[80:81], v[80:81], v[80:81]
	v_mul_f32_e32 v10, v24, v24
	v_pk_fma_f32 v[78:79], v[78:79], v[78:79], v[80:81]
	v_pk_fma_f32 v[80:81], v[24:25], v[24:25], v[10:11] op_sel_hi:[1,1,0]
	v_mul_f32_e32 v10, v26, v26
	v_pk_add_f32 v[22:23], v[22:23], v[22:23] op_sel_hi:[0,1]
	v_pk_add_f32 v[78:79], v[78:79], v[78:79] op_sel_hi:[0,1]
	v_pk_fma_f32 v[82:83], v[26:27], v[26:27], v[10:11] op_sel_hi:[1,1,0]
	v_pk_mul_f32 v[100:101], v[28:29], v[28:29]
	v_pk_mul_f32 v[102:103], v[30:31], v[30:31]
	v_mov_b32_e32 v80, v100
	v_mov_b32_e32 v82, v101
	v_mov_b32_e32 v78, v102
	v_mov_b32_e32 v22, v103
	v_pk_add_f32 v[80:81], v[80:81], v[82:83]
	v_pk_add_f32 v[22:23], v[78:79], v[22:23]
	s_nop 0
	v_pk_add_f32 v[22:23], v[80:81], v[22:23]
	s_nop 0
	v_add_f32_e32 v10, v22, v23
	ds_bpermute_b32 v22, v1, v10
	s_waitcnt lgkmcnt(0)
	v_add_f32_e32 v10, v10, v22
	ds_bpermute_b32 v22, v84, v10
	s_waitcnt lgkmcnt(0)
	v_add_f32_e32 v10, v10, v22
	ds_bpermute_b32 v22, v85, v10
	s_waitcnt lgkmcnt(0)
	v_add_f32_e32 v10, v10, v22
	ds_bpermute_b32 v22, v86, v10
	s_waitcnt lgkmcnt(0)
	v_add_f32_e32 v10, v10, v22
	ds_bpermute_b32 v22, v87, v10
	s_waitcnt lgkmcnt(0)
	v_add_f32_e32 v10, v10, v22
	ds_bpermute_b32 v22, v88, v10
	s_waitcnt lgkmcnt(0)
	v_add_f32_e32 v10, v10, v22
	v_fmamk_f32 v10, v10, 0x39800000, v97
	v_mul_f32_e32 v22, 0x4f800000, v10
	v_cmp_gt_f32_e32 vcc, s11, v10
	s_nop 1
	v_cndmask_b32_e32 v10, v10, v22, vcc
	v_sqrt_f32_e32 v22, v10
	s_nop 0
	v_add_u32_e32 v23, -1, v22
	v_fma_f32 v82, -v23, v22, v10
	v_cmp_ge_f32_e64 s[0:1], 0, v82
	v_add_u32_e32 v82, 1, v22
	s_nop 0
	v_cndmask_b32_e64 v23, v22, v23, s[0:1]
	v_fma_f32 v22, -v82, v22, v10
	v_cmp_lt_f32_e64 s[0:1], 0, v22
	s_nop 1
	v_cndmask_b32_e64 v22, v23, v82, s[0:1]
	v_mul_f32_e32 v23, 0x37800000, v22
	v_cndmask_b32_e32 v22, v22, v23, vcc
	v_cmp_class_f32_e32 vcc, v10, v98
	s_nop 1
	v_cndmask_b32_e32 v10, v22, v10, vcc
	v_div_scale_f32 v22, s[0:1], v10, v10, 1.0
	v_rcp_f32_e32 v23, v22
	s_lshr_b32 s0, s8, 13
	s_mul_i32 s0, s0, 0xc000
	s_add_i32 s0, s0, 0
	v_fma_f32 v82, -v22, v23, 1.0
	v_fmac_f32_e32 v23, v82, v23
	v_div_scale_f32 v82, vcc, 1.0, v10, 1.0
	v_mul_f32_e32 v83, v82, v23
	v_fma_f32 v100, -v22, v83, v82
	v_fmac_f32_e32 v83, v100, v23
	v_lshl_add_u32 v100, v89, 4, s0
	ds_read_b128 v[102:105], v100
	ds_read_b128 v[106:109], v100 offset:16
	v_fma_f32 v22, -v22, v83, v82
	v_div_fmas_f32 v22, v22, v23, v83
	v_div_fixup_f32 v10, v22, v10, 1.0
	v_pk_mul_f32 v[18:19], v[18:19], v[10:11] op_sel_hi:[1,0]
	v_pk_mul_f32 v[20:21], v[20:21], v[10:11] op_sel_hi:[1,0]
	s_waitcnt vmcnt(15) lgkmcnt(1)
	v_pk_fma_f32 v[22:23], v[102:103], v[18:19], v[130:131]
	v_pk_fma_f32 v[20:21], v[104:105], v[20:21], v[132:133]
	v_add_co_u32_e32 v18, vcc, s30, v32
	v_cvt_pk_f16_f32 v78, v22, v23
	v_cvt_pk_f16_f32 v79, v20, v21
	v_addc_co_u32_e32 v19, vcc, 0, v33, vcc
	global_store_dwordx2 v[18:19], v[78:79], off offset:-4096
	s_nop 0
	v_add_co_u32_e32 v110, vcc, s27, v32
	v_pk_mul_f32 v[34:35], v[34:35], v[10:11] op_sel_hi:[1,0]
	s_nop 0
	v_addc_co_u32_e32 v111, vcc, 0, v33, vcc
	v_pk_mul_f32 v[32:33], v[76:77], v[10:11] op_sel_hi:[1,0]
	v_lshl_add_u32 v101, v90, 4, s0
	v_pk_mul_f32 v[114:115], v[44:45], v[10:11] op_sel_hi:[1,0]
	v_pk_mul_f32 v[44:45], v[46:47], v[10:11] op_sel_hi:[1,0]
	v_lshl_add_u32 v164, v93, 4, s0
	v_lshl_add_u32 v165, v94, 4, s0
	v_lshl_add_u32 v167, v95, 4, s0
	v_pk_mul_f32 v[6:7], v[6:7], v[10:11] op_sel_hi:[1,0]
	v_pk_mul_f32 v[8:9], v[8:9], v[10:11] op_sel_hi:[1,0]
	v_pk_mul_f32 v[2:3], v[2:3], v[10:11] op_sel_hi:[1,0]
	v_pk_mul_f32 v[4:5], v[4:5], v[10:11] op_sel_hi:[1,0]
	v_pk_mul_f32 v[118:119], v[28:29], v[10:11] op_sel_hi:[1,0]
	v_pk_mul_f32 v[120:121], v[30:31], v[10:11] op_sel_hi:[1,0]
	v_pk_mul_f32 v[28:29], v[20:21], v[20:21]
	v_pk_mul_f32 v[30:31], v[22:23], v[22:23]
	v_lshl_add_u32 v220, v96, 4, s0
	v_pk_mov_b32 v[122:123], v[30:31], v[28:29] op_sel:[1,0]
	v_mov_b32_e32 v31, v29
	v_pk_add_f32 v[28:29], v[122:123], v[30:31]
	v_pk_mul_f32 v[24:25], v[24:25], v[10:11] op_sel_hi:[1,0]
	v_pk_add_f32 v[122:123], v[28:29], v[28:29] op_sel_hi:[0,1]
	v_pk_mul_f32 v[26:27], v[26:27], v[10:11] op_sel_hi:[1,0]
	s_waitcnt vmcnt(15) lgkmcnt(0)
	v_pk_fma_f32 v[32:33], v[108:109], v[32:33], v[136:137]
	v_pk_fma_f32 v[34:35], v[106:107], v[34:35], v[134:135]
	v_cvt_pk_f16_f32 v77, v32, v33
	v_cvt_pk_f16_f32 v76, v34, v35
	global_store_dwordx2 v[110:111], v[76:77], off offset:8
	s_nop 0
	ds_read_b128 v[80:83], v101
	ds_read_b128 v[102:105], v101 offset:16
	v_pk_mul_f32 v[106:107], v[36:37], v[10:11] op_sel_hi:[1,0]
	v_pk_mul_f32 v[36:37], v[38:39], v[10:11] op_sel_hi:[1,0]
	v_add_co_u32_e32 v108, vcc, s29, v16
	v_pk_mul_f32 v[28:29], v[34:35], v[34:35]
	s_nop 0
	v_addc_co_u32_e32 v109, vcc, 0, v17, vcc
	v_add_co_u32_e32 v112, vcc, s28, v16
	v_pk_mul_f32 v[30:31], v[32:33], v[32:33]
	s_nop 0
	v_addc_co_u32_e32 v113, vcc, 0, v17, vcc
	v_add_co_u32_e32 v116, vcc, s31, v16
	v_pk_mov_b32 v[124:125], v[28:29], v[30:31] op_sel:[1,0]
	s_nop 0
	v_addc_co_u32_e32 v117, vcc, 0, v17, vcc
	v_mov_b32_e32 v29, v31
	v_pk_add_f32 v[28:29], v[124:125], v[28:29]
	s_waitcnt vmcnt(15) lgkmcnt(1)
	v_pk_fma_f32 v[36:37], v[82:83], v[36:37], v[140:141]
	v_pk_fma_f32 v[38:39], v[80:81], v[106:107], v[138:139]
	v_cvt_pk_f16_f32 v77, v36, v37
	v_cvt_pk_f16_f32 v76, v38, v39
	global_store_dwordx2 v[110:111], v[76:77], off offset:1024
	s_nop 0
	v_pk_mul_f32 v[80:81], v[40:41], v[10:11] op_sel_hi:[1,0]
	v_pk_mul_f32 v[40:41], v[42:43], v[10:11] op_sel_hi:[1,0]
	v_pk_add_f32 v[124:125], v[28:29], v[28:29] op_sel_hi:[0,1]
	v_mul_f32_e32 v28, v36, v36
	v_pk_fma_f32 v[128:129], v[36:37], v[36:37], v[28:29] op_sel_hi:[1,1,0]
	s_waitcnt vmcnt(15) lgkmcnt(0)
	v_pk_fma_f32 v[40:41], v[104:105], v[40:41], v[144:145]
	v_pk_fma_f32 v[42:43], v[102:103], v[80:81], v[142:143]
	v_cvt_pk_f16_f32 v77, v40, v41
	v_cvt_pk_f16_f32 v76, v42, v43
	global_store_dwordx2 v[110:111], v[76:77], off offset:1032
	s_nop 0
	v_lshl_add_u32 v102, v91, 4, s0
	ds_read_b128 v[80:83], v102
	ds_read_b128 v[104:107], v102 offset:16
	v_lshl_add_u32 v103, v92, 4, s0
	v_mul_f32_e32 v128, v43, v43
	v_mul_f32_e32 v122, v40, v40
	v_mul_f32_e32 v124, v41, v41
	s_waitcnt vmcnt(15) lgkmcnt(1)
	v_pk_fma_f32 v[44:45], v[82:83], v[44:45], v[148:149]
	v_pk_fma_f32 v[46:47], v[80:81], v[114:115], v[146:147]
	v_cvt_pk_f16_f32 v77, v44, v45
	v_cvt_pk_f16_f32 v76, v46, v47
	global_store_dwordx2 v[110:111], v[76:77], off offset:2048
	s_nop 0
	v_pk_mul_f32 v[80:81], v[48:49], v[10:11] op_sel_hi:[1,0]
	v_pk_mul_f32 v[48:49], v[50:51], v[10:11] op_sel_hi:[1,0]
	v_pk_mul_f32 v[114:115], v[60:61], v[10:11] op_sel_hi:[1,0]
	v_pk_mul_f32 v[60:61], v[62:63], v[10:11] op_sel_hi:[1,0]
	s_waitcnt vmcnt(15) lgkmcnt(0)
	v_pk_fma_f32 v[48:49], v[106:107], v[48:49], v[152:153]
	v_pk_fma_f32 v[50:51], v[104:105], v[80:81], v[150:151]
	v_cvt_pk_f16_f32 v77, v48, v49
	v_cvt_pk_f16_f32 v76, v50, v51
	global_store_dwordx2 v[110:111], v[76:77], off offset:2056
	s_nop 0
	ds_read_b128 v[80:83], v103
	ds_read_b128 v[104:107], v103 offset:16
	s_waitcnt vmcnt(15) lgkmcnt(1)
	v_pk_fma_f32 v[60:61], v[82:83], v[60:61], v[156:157]
	v_pk_fma_f32 v[62:63], v[80:81], v[114:115], v[154:155]
	v_cvt_pk_f16_f32 v77, v60, v61
	v_cvt_pk_f16_f32 v76, v62, v63
	global_store_dwordx2 v[110:111], v[76:77], off offset:3072
	s_nop 0
	v_pk_mul_f32 v[80:81], v[64:65], v[10:11] op_sel_hi:[1,0]
	v_pk_mul_f32 v[64:65], v[66:67], v[10:11] op_sel_hi:[1,0]
	s_waitcnt vmcnt(15) lgkmcnt(0)
	v_pk_fma_f32 v[66:67], v[80:81], v[104:105], v[158:159]
	v_pk_fma_f32 v[64:65], v[64:65], v[106:107], v[160:161]
	v_cvt_pk_f16_f32 v76, v66, v67
	v_cvt_pk_f16_f32 v77, v64, v65
	global_store_dwordx2 v[110:111], v[76:77], off offset:3080
	s_nop 0
	ds_read_b128 v[80:83], v164
	ds_read_b128 v[104:107], v164 offset:16
	v_pk_mul_f32 v[110:111], v[68:69], v[10:11] op_sel_hi:[1,0]
	v_pk_mul_f32 v[68:69], v[70:71], v[10:11] op_sel_hi:[1,0]
	s_waitcnt vmcnt(15) lgkmcnt(1)
	v_pk_fma_f32 v[70:71], v[110:111], v[80:81], v[168:169]
	v_pk_fma_f32 v[68:69], v[68:69], v[82:83], v[170:171]
	v_cvt_pk_f16_f32 v76, v70, v71
	v_cvt_pk_f16_f32 v77, v68, v69
	global_store_dwordx2 v[18:19], v[76:77], off
	s_nop 0
	v_pk_mul_f32 v[80:81], v[72:73], v[10:11] op_sel_hi:[1,0]
	v_pk_mul_f32 v[72:73], v[74:75], v[10:11] op_sel_hi:[1,0]
	v_pk_mul_f32 v[110:111], v[56:57], v[10:11] op_sel_hi:[1,0]
	v_pk_mul_f32 v[56:57], v[58:59], v[10:11] op_sel_hi:[1,0]
	s_waitcnt vmcnt(15) lgkmcnt(0)
	v_pk_fma_f32 v[72:73], v[72:73], v[106:107], v[174:175]
	v_pk_fma_f32 v[74:75], v[80:81], v[104:105], v[172:173]
	v_cvt_pk_f16_f32 v77, v72, v73
	v_cvt_pk_f16_f32 v76, v74, v75
	global_store_dwordx2 v[18:19], v[76:77], off offset:8
	s_nop 0
	ds_read_b128 v[80:83], v165
	ds_read_b128 v[104:107], v165 offset:16
	s_waitcnt vmcnt(15) lgkmcnt(1)
	v_pk_fma_f32 v[56:57], v[56:57], v[82:83], v[178:179]
	v_pk_fma_f32 v[58:59], v[110:111], v[80:81], v[176:177]
	v_cvt_pk_f16_f32 v77, v56, v57
	v_cvt_pk_f16_f32 v76, v58, v59
	global_store_dwordx2 v[18:19], v[76:77], off offset:1024
	s_nop 0
	v_pk_mul_f32 v[80:81], v[52:53], v[10:11] op_sel_hi:[1,0]
	v_pk_mul_f32 v[52:53], v[54:55], v[10:11] op_sel_hi:[1,0]
	v_mul_f32_e32 v10, v38, v38
	v_pk_fma_f32 v[126:127], v[38:39], v[38:39], v[10:11] op_sel_hi:[1,1,0]
	v_mul_f32_e32 v10, v50, v50
	v_mul_f32_e32 v126, v42, v42
	s_waitcnt vmcnt(15) lgkmcnt(0)
	v_pk_fma_f32 v[52:53], v[52:53], v[106:107], v[182:183]
	v_pk_fma_f32 v[54:55], v[80:81], v[104:105], v[180:181]
	v_cvt_pk_f16_f32 v77, v52, v53
	v_cvt_pk_f16_f32 v76, v54, v55
	global_store_dwordx2 v[18:19], v[76:77], off offset:1032
	s_nop 0
	ds_read_b128 v[104:107], v167
	ds_read_b128 v[108:111], v167 offset:16
	s_waitcnt vmcnt(15) lgkmcnt(1)
	v_pk_fma_f32 v[76:77], v[8:9], v[106:107], v[186:187]
	v_pk_fma_f32 v[78:79], v[6:7], v[104:105], v[184:185]
	v_cvt_pk_f16_f32 v7, v76, v77
	v_cvt_pk_f16_f32 v6, v78, v79
	global_store_dwordx2 v[18:19], v[6:7], off offset:2048
	s_nop 0
	s_waitcnt vmcnt(15) lgkmcnt(0)
	v_pk_fma_f32 v[80:81], v[4:5], v[110:111], v[190:191]
	v_pk_fma_f32 v[82:83], v[2:3], v[108:109], v[188:189]
	v_cvt_pk_f16_f32 v3, v80, v81
	v_cvt_pk_f16_f32 v2, v82, v83
	global_store_dwordx2 v[18:19], v[2:3], off offset:2056
	s_nop 0
	ds_read_b128 v[108:111], v220
	ds_read_b128 v[112:115], v220 offset:16
	ds_read_b128 v[6:9], v100 offset:16384
	ds_read_b128 v[2:5], v100 offset:16400
	s_waitcnt vmcnt(15) lgkmcnt(3)
	v_pk_fma_f32 v[28:29], v[26:27], v[110:111], v[194:195]
	v_pk_fma_f32 v[30:31], v[24:25], v[108:109], v[192:193]
	v_cvt_pk_f16_f32 v25, v28, v29
	v_cvt_pk_f16_f32 v24, v30, v31
	global_store_dwordx2 v[18:19], v[24:25], off offset:3072
	s_nop 0
	v_pk_add_f32 v[24:25], v[126:127], v[128:129]
	v_pk_add_f32 v[26:27], v[122:123], v[124:125]
	v_pk_mul_f32 v[108:109], v[44:45], v[44:45]
	v_pk_add_f32 v[24:25], v[24:25], v[26:27]
	v_pk_mul_f32 v[26:27], v[46:47], v[46:47]
	v_pk_add_f32 v[24:25], v[24:25], v[24:25] op_sel_hi:[0,1]
	v_pk_mov_b32 v[110:111], v[26:27], v[108:109] op_sel:[1,0]
	v_mov_b32_e32 v27, v109
	v_pk_add_f32 v[26:27], v[110:111], v[26:27]
	v_mul_f32_e32 v24, v48, v48
	v_pk_add_f32 v[26:27], v[26:27], v[26:27] op_sel_hi:[0,1]
	v_pk_fma_f32 v[108:109], v[50:51], v[50:51], v[10:11] op_sel_hi:[1,1,0]
	v_pk_fma_f32 v[110:111], v[48:49], v[48:49], v[24:25] op_sel_hi:[1,1,0]
	v_mul_f32_e32 v108, v62, v62
	v_mul_f32_e32 v110, v63, v63
	v_mul_f32_e32 v26, v60, v60
	v_mul_f32_e32 v24, v61, v61
	v_pk_add_f32 v[108:109], v[108:109], v[110:111]
	v_pk_add_f32 v[24:25], v[26:27], v[24:25]
	v_pk_mul_f32 v[26:27], v[66:67], v[66:67]
	v_pk_add_f32 v[24:25], v[108:109], v[24:25]
	v_pk_mul_f32 v[108:109], v[64:65], v[64:65]
	v_mul_f32_e32 v10, v71, v71
	v_pk_mov_b32 v[110:111], v[26:27], v[108:109] op_sel:[1,0]
	v_mov_b32_e32 v27, v109
	v_pk_add_f32 v[26:27], v[110:111], v[26:27]
	v_mul_f32_e32 v108, v69, v69
	v_pk_add_f32 v[24:25], v[24:25], v[24:25] op_sel:[0,1] op_sel_hi:[1,0]
	v_pk_add_f32 v[26:27], v[26:27], v[26:27] op_sel:[0,1] op_sel_hi:[1,0]
	v_pk_fma_f32 v[110:111], v[70:71], v[70:71], v[10:11] op_sel_hi:[1,1,0]
	v_pk_fma_f32 v[108:109], v[68:69], v[68:69], v[108:109] op_sel_hi:[1,1,0]
	v_mul_f32_e32 v116, v73, v73
	v_mul_f32_e32 v111, v74, v74
	v_mul_f32_e32 v109, v75, v75
	v_mul_f32_e32 v27, v72, v72
	v_mov_b32_e32 v25, v116
	v_pk_add_f32 v[108:109], v[110:111], v[108:109]
	v_pk_add_f32 v[24:25], v[26:27], v[24:25]
	v_pk_mul_f32 v[26:27], v[58:59], v[58:59]
	v_pk_add_f32 v[24:25], v[108:109], v[24:25]
	v_pk_mul_f32 v[108:109], v[56:57], v[56:57]
	v_mul_f32_e32 v10, v55, v55
	v_pk_mov_b32 v[110:111], v[26:27], v[108:109] op_sel:[1,0]
	v_mov_b32_e32 v27, v109
	v_pk_add_f32 v[26:27], v[110:111], v[26:27]
	v_mul_f32_e32 v108, v53, v53
	v_pk_add_f32 v[24:25], v[24:25], v[24:25] op_sel:[0,1] op_sel_hi:[1,0]
	v_pk_add_f32 v[26:27], v[26:27], v[26:27] op_sel:[0,1] op_sel_hi:[1,0]
	v_pk_fma_f32 v[110:111], v[54:55], v[54:55], v[10:11] op_sel_hi:[1,1,0]
	v_pk_fma_f32 v[108:109], v[52:53], v[52:53], v[108:109] op_sel_hi:[1,1,0]
	v_mul_f32_e32 v116, v77, v77
	v_mul_f32_e32 v25, v78, v78
	v_mul_f32_e32 v27, v79, v79
	v_mul_f32_e32 v111, v76, v76
	v_mov_b32_e32 v109, v116
	v_pk_add_f32 v[24:25], v[24:25], v[26:27]
	v_pk_add_f32 v[26:27], v[110:111], v[108:109]
	v_mul_f32_e32 v10, v31, v31
	v_pk_add_f32 v[24:25], v[24:25], v[26:27]
	v_pk_mul_f32 v[26:27], v[80:81], v[80:81]
	v_pk_add_f32 v[108:109], v[24:25], v[24:25] op_sel:[0,1] op_sel_hi:[1,0]
	v_pk_mul_f32 v[24:25], v[82:83], v[82:83]
	v_pk_fma_f32 v[116:117], v[30:31], v[30:31], v[10:11] op_sel_hi:[1,1,0]
	v_pk_mov_b32 v[110:111], v[24:25], v[26:27] op_sel:[1,0]
	v_mov_b32_e32 v25, v27
	v_pk_add_f32 v[24:25], v[110:111], v[24:25]
	s_waitcnt vmcnt(15) lgkmcnt(2)
	v_pk_fma_f32 v[26:27], v[118:119], v[112:113], v[196:197]
	v_pk_add_f32 v[110:111], v[24:25], v[24:25] op_sel:[0,1] op_sel_hi:[1,0]
	v_mul_f32_e32 v24, v29, v29
	v_pk_fma_f32 v[122:123], v[28:29], v[28:29], v[24:25] op_sel_hi:[1,1,0]
	v_pk_fma_f32 v[24:25], v[120:121], v[114:115], v[198:199]
	v_mul_f32_e32 v109, v26, v26
	v_mul_f32_e32 v111, v27, v27
	v_mul_f32_e32 v117, v24, v24
	v_mul_f32_e32 v123, v25, v25
	v_pk_add_f32 v[104:105], v[108:109], v[110:111]
	v_pk_add_f32 v[106:107], v[116:117], v[122:123]
	s_nop 0
	v_pk_add_f32 v[104:105], v[104:105], v[106:107]
	s_nop 0
	v_add_f32_e32 v10, v104, v105
	ds_bpermute_b32 v120, v1, v10
	ds_read_b128 v[104:107], v100 offset:32768
	ds_read_b128 v[108:111], v100 offset:32784
	ds_read_b128 v[112:115], v101 offset:16384
	ds_read_b128 v[116:119], v101 offset:16400
	s_waitcnt lgkmcnt(4)
	v_add_f32_e32 v10, v10, v120
	ds_bpermute_b32 v100, v84, v10
	ds_read_b128 v[120:123], v101 offset:32768
	ds_read_b128 v[124:127], v101 offset:32784
	ds_read_b128 v[128:131], v102 offset:16384
	ds_read_b128 v[132:135], v102 offset:16400
	ds_read_b128 v[136:139], v102 offset:32768
	ds_read_b128 v[140:143], v102 offset:32784
	ds_read_b128 v[144:147], v103 offset:16384
	ds_read_b128 v[148:151], v103 offset:16400
	s_waitcnt lgkmcnt(8)
	v_add_f32_e32 v10, v10, v100
	ds_bpermute_b32 v100, v85, v10
	s_waitcnt lgkmcnt(0)
	v_add_f32_e32 v10, v10, v100
	ds_bpermute_b32 v168, v86, v10
	ds_read_b128 v[152:155], v103 offset:32768
	ds_read_b128 v[100:103], v103 offset:32784
	ds_read_b128 v[156:159], v164 offset:16384
	ds_read_b128 v[160:163], v164 offset:16400
	s_waitcnt lgkmcnt(4)
	v_add_f32_e32 v10, v10, v168
	ds_bpermute_b32 v184, v87, v10
	ds_read_b128 v[168:171], v164 offset:32768
	ds_read_b128 v[172:175], v164 offset:32784
	ds_read_b128 v[176:179], v165 offset:16384
	ds_read_b128 v[180:183], v165 offset:16400
	s_waitcnt lgkmcnt(4)
	v_add_f32_e32 v10, v10, v184
	ds_bpermute_b32 v164, v88, v10
	ds_read_b128 v[184:187], v165 offset:32768
	ds_read_b128 v[188:191], v165 offset:32784
	ds_read_b128 v[192:195], v167 offset:16384
	ds_read_b128 v[196:199], v167 offset:16400
	ds_read_b128 v[200:203], v167 offset:32768
	ds_read_b128 v[204:207], v167 offset:32784
	ds_read_b128 v[208:211], v220 offset:16384
	ds_read_b128 v[212:215], v220 offset:16400
	s_waitcnt lgkmcnt(8)
	v_add_f32_e32 v10, v10, v164
	v_fmamk_f32 v10, v10, 0x39800000, v97
	v_mul_f32_e32 v164, 0x4f800000, v10
	v_cmp_gt_f32_e32 vcc, s11, v10
	s_nop 1
	v_cndmask_b32_e32 v10, v10, v164, vcc
	v_sqrt_f32_e32 v164, v10
	s_nop 0
	v_add_u32_e32 v165, -1, v164
	v_add_u32_e32 v167, 1, v164
	v_fma_f32 v216, -v165, v164, v10
	v_fma_f32 v217, -v167, v164, v10
	v_cmp_ge_f32_e64 s[0:1], 0, v216
	s_nop 1
	v_cndmask_b32_e64 v164, v164, v165, s[0:1]
	v_cmp_lt_f32_e64 s[0:1], 0, v217
	ds_read_b128 v[216:219], v220 offset:32768
	ds_read_b128 v[220:223], v220 offset:32784
	v_cndmask_b32_e64 v164, v164, v167, s[0:1]
	v_mul_f32_e32 v165, 0x37800000, v164
	v_cndmask_b32_e32 v164, v164, v165, vcc
	v_cmp_class_f32_e32 vcc, v10, v98
	s_nop 1
	v_cndmask_b32_e32 v10, v164, v10, vcc
	v_div_scale_f32 v164, s[0:1], v10, v10, 1.0
	v_rcp_f32_e32 v165, v164
	v_div_scale_f32 v167, vcc, 1.0, v10, 1.0
	s_and_b32 s0, s8, 0xfe
	v_fma_f32 v224, -v164, v165, 1.0
	v_fmac_f32_e32 v165, v224, v165
	v_mul_f32_e32 v224, v167, v165
	v_fma_f32 v225, -v164, v224, v167
	v_fmac_f32_e32 v224, v225, v165
	v_fma_f32 v164, -v164, v224, v167
	v_div_fmas_f32 v164, v164, v165, v224
	v_div_fixup_f32 v10, v164, v10, 1.0
	v_pk_mul_f32 v[22:23], v[22:23], v[10:11] op_sel_hi:[1,0]
	v_pk_mul_f32 v[20:21], v[20:21], v[10:11] op_sel_hi:[1,0]
	v_pk_mul_f32 v[34:35], v[34:35], v[10:11] op_sel_hi:[1,0]
	v_pk_mul_f32 v[32:33], v[32:33], v[10:11] op_sel_hi:[1,0]
	v_pk_mul_f32 v[38:39], v[38:39], v[10:11] op_sel_hi:[1,0]
	v_pk_mul_f32 v[36:37], v[36:37], v[10:11] op_sel_hi:[1,0]
	v_pk_mul_f32 v[42:43], v[42:43], v[10:11] op_sel_hi:[1,0]
	v_pk_mul_f32 v[40:41], v[40:41], v[10:11] op_sel_hi:[1,0]
	v_pk_mul_f32 v[46:47], v[46:47], v[10:11] op_sel_hi:[1,0]
	v_pk_mul_f32 v[44:45], v[44:45], v[10:11] op_sel_hi:[1,0]
	v_pk_mul_f32 v[50:51], v[50:51], v[10:11] op_sel_hi:[1,0]
	v_pk_mul_f32 v[48:49], v[48:49], v[10:11] op_sel_hi:[1,0]
	v_pk_mul_f32 v[62:63], v[62:63], v[10:11] op_sel_hi:[1,0]
	v_pk_mul_f32 v[60:61], v[60:61], v[10:11] op_sel_hi:[1,0]
	v_pk_mul_f32 v[66:67], v[66:67], v[10:11] op_sel_hi:[1,0]
	v_pk_mul_f32 v[64:65], v[64:65], v[10:11] op_sel_hi:[1,0]
	v_pk_mul_f32 v[70:71], v[70:71], v[10:11] op_sel_hi:[1,0]
	v_pk_mul_f32 v[68:69], v[68:69], v[10:11] op_sel_hi:[1,0]
	v_pk_mul_f32 v[74:75], v[74:75], v[10:11] op_sel_hi:[1,0]
	v_pk_mul_f32 v[72:73], v[72:73], v[10:11] op_sel_hi:[1,0]
	v_pk_mul_f32 v[58:59], v[58:59], v[10:11] op_sel_hi:[1,0]
	v_pk_mul_f32 v[56:57], v[56:57], v[10:11] op_sel_hi:[1,0]
	v_pk_mul_f32 v[54:55], v[54:55], v[10:11] op_sel_hi:[1,0]
	v_pk_mul_f32 v[52:53], v[52:53], v[10:11] op_sel_hi:[1,0]
	v_pk_mul_f32 v[78:79], v[78:79], v[10:11] op_sel_hi:[1,0]
	v_pk_mul_f32 v[76:77], v[76:77], v[10:11] op_sel_hi:[1,0]
	v_pk_mul_f32 v[82:83], v[82:83], v[10:11] op_sel_hi:[1,0]
	v_pk_mul_f32 v[80:81], v[80:81], v[10:11] op_sel_hi:[1,0]
	v_pk_mul_f32 v[30:31], v[30:31], v[10:11] op_sel_hi:[1,0]
	v_pk_mul_f32 v[28:29], v[28:29], v[10:11] op_sel_hi:[1,0]
	v_pk_mul_f32 v[164:165], v[26:27], v[10:11] op_sel_hi:[1,0]
	v_pk_mul_f32 v[224:225], v[24:25], v[10:11] op_sel_hi:[1,0]
	v_pk_fma_f32 v[8:9], v[8:9], v[20:21], v[106:107]
	v_pk_fma_f32 v[6:7], v[6:7], v[22:23], v[104:105]
	v_pk_fma_f32 v[4:5], v[4:5], v[32:33], v[110:111]
	v_pk_fma_f32 v[2:3], v[2:3], v[34:35], v[108:109]
	v_pk_fma_f32 v[20:21], v[114:115], v[36:37], v[122:123]
	v_pk_fma_f32 v[22:23], v[112:113], v[38:39], v[120:121]
	v_pk_fma_f32 v[32:33], v[118:119], v[40:41], v[126:127]
	v_pk_fma_f32 v[34:35], v[116:117], v[42:43], v[124:125]
	v_pk_fma_f32 v[36:37], v[130:131], v[44:45], v[138:139]
	v_pk_fma_f32 v[38:39], v[128:129], v[46:47], v[136:137]
	v_pk_fma_f32 v[40:41], v[134:135], v[48:49], v[142:143]
	v_pk_fma_f32 v[42:43], v[132:133], v[50:51], v[140:141]
	v_pk_fma_f32 v[44:45], v[60:61], v[146:147], v[154:155]
	v_pk_fma_f32 v[46:47], v[62:63], v[144:145], v[152:153]
	v_pk_fma_f32 v[48:49], v[64:65], v[150:151], v[102:103]
	v_pk_fma_f32 v[50:51], v[66:67], v[148:149], v[100:101]
	v_pk_fma_f32 v[60:61], v[68:69], v[158:159], v[170:171]
	v_pk_fma_f32 v[62:63], v[70:71], v[156:157], v[168:169]
	v_pk_fma_f32 v[64:65], v[72:73], v[162:163], v[174:175]
	v_pk_fma_f32 v[66:67], v[74:75], v[160:161], v[172:173]
	s_waitcnt lgkmcnt(9)
	v_pk_fma_f32 v[56:57], v[56:57], v[178:179], v[186:187]
	v_pk_fma_f32 v[58:59], v[58:59], v[176:177], v[184:185]
	s_waitcnt lgkmcnt(8)
	v_pk_fma_f32 v[52:53], v[52:53], v[182:183], v[190:191]
	v_pk_fma_f32 v[54:55], v[54:55], v[180:181], v[188:189]
	s_waitcnt lgkmcnt(5)
	v_pk_fma_f32 v[68:69], v[76:77], v[194:195], v[202:203]
	v_pk_fma_f32 v[70:71], v[78:79], v[192:193], v[200:201]
	s_waitcnt lgkmcnt(4)
	v_pk_fma_f32 v[72:73], v[80:81], v[198:199], v[206:207]
	v_pk_fma_f32 v[74:75], v[82:83], v[196:197], v[204:205]
	s_waitcnt lgkmcnt(1)
	v_pk_fma_f32 v[28:29], v[28:29], v[210:211], v[218:219]
	v_pk_fma_f32 v[30:31], v[30:31], v[208:209], v[216:217]
	s_waitcnt lgkmcnt(0)
	v_pk_fma_f32 v[76:77], v[224:225], v[214:215], v[222:223]
	v_pk_fma_f32 v[78:79], v[164:165], v[212:213], v[220:221]
	v_add_f32_e32 v10, v6, v7
	v_sub_f32_e32 v6, v6, v7
	v_add_f32_e32 v7, v8, v9
	v_sub_f32_e32 v8, v8, v9
	v_add_f32_e32 v9, v2, v3
	v_sub_f32_e32 v2, v2, v3
	v_add_f32_e32 v3, v4, v5
	v_sub_f32_e32 v4, v4, v5
	v_add_f32_e32 v5, v22, v23
	v_sub_f32_e32 v22, v22, v23
	v_add_f32_e32 v23, v20, v21
	v_sub_f32_e32 v20, v20, v21
	v_add_f32_e32 v21, v34, v35
	v_sub_f32_e32 v34, v34, v35
	v_add_f32_e32 v35, v32, v33
	v_sub_f32_e32 v32, v32, v33
	v_add_f32_e32 v33, v38, v39
	v_sub_f32_e32 v38, v38, v39
	v_add_f32_e32 v39, v36, v37
	v_sub_f32_e32 v36, v36, v37
	v_add_f32_e32 v37, v42, v43
	v_sub_f32_e32 v42, v42, v43
	v_add_f32_e32 v43, v40, v41
	v_sub_f32_e32 v40, v40, v41
	v_add_f32_e32 v41, v46, v47
	v_sub_f32_e32 v46, v46, v47
	v_add_f32_e32 v47, v44, v45
	v_sub_f32_e32 v44, v44, v45
	v_add_f32_e32 v45, v50, v51
	v_sub_f32_e32 v50, v50, v51
	v_add_f32_e32 v51, v48, v49
	v_sub_f32_e32 v48, v48, v49
	v_add_f32_e32 v49, v62, v63
	v_sub_f32_e32 v62, v62, v63
	v_add_f32_e32 v63, v60, v61
	v_sub_f32_e32 v60, v60, v61
	v_add_f32_e32 v61, v66, v67
	v_sub_f32_e32 v66, v66, v67
	v_add_f32_e32 v67, v64, v65
	v_sub_f32_e32 v64, v64, v65
	v_add_f32_e32 v65, v58, v59
	v_sub_f32_e32 v58, v58, v59
	v_add_f32_e32 v59, v56, v57
	v_sub_f32_e32 v56, v56, v57
	v_add_f32_e32 v57, v54, v55
	v_sub_f32_e32 v54, v54, v55
	v_add_f32_e32 v55, v52, v53
	v_sub_f32_e32 v52, v52, v53
	v_add_f32_e32 v53, v70, v71
	v_sub_f32_e32 v70, v70, v71
	v_add_f32_e32 v71, v68, v69
	v_sub_f32_e32 v68, v68, v69
	v_add_f32_e32 v69, v74, v75
	v_sub_f32_e32 v74, v74, v75
	v_add_f32_e32 v75, v72, v73
	v_sub_f32_e32 v72, v72, v73
	v_add_f32_e32 v73, v30, v31
	v_sub_f32_e32 v30, v30, v31
	v_add_f32_e32 v31, v28, v29
	v_sub_f32_e32 v28, v28, v29
	v_add_f32_e32 v29, v78, v79
	v_sub_f32_e32 v78, v78, v79
	v_add_f32_e32 v79, v76, v77
	v_sub_f32_e32 v76, v76, v77
	v_add_f32_e32 v77, v10, v7
	v_sub_f32_e32 v7, v10, v7
	v_add_f32_e32 v10, v6, v8
	v_sub_f32_e32 v6, v6, v8
	v_add_f32_e32 v8, v9, v3
	v_sub_f32_e32 v3, v9, v3
	v_add_f32_e32 v9, v2, v4
	v_sub_f32_e32 v2, v2, v4
	v_add_f32_e32 v4, v5, v23
	v_sub_f32_e32 v5, v5, v23
	v_add_f32_e32 v23, v22, v20
	v_sub_f32_e32 v20, v22, v20
	v_add_f32_e32 v22, v21, v35
	v_sub_f32_e32 v21, v21, v35
	v_add_f32_e32 v35, v34, v32
	v_sub_f32_e32 v32, v34, v32
	v_add_f32_e32 v34, v33, v39
	v_sub_f32_e32 v33, v33, v39
	v_add_f32_e32 v39, v38, v36
	v_sub_f32_e32 v36, v38, v36
	v_add_f32_e32 v38, v37, v43
	v_sub_f32_e32 v37, v37, v43
	v_add_f32_e32 v43, v42, v40
	v_sub_f32_e32 v40, v42, v40
	v_add_f32_e32 v42, v41, v47
	v_sub_f32_e32 v41, v41, v47
	v_add_f32_e32 v47, v46, v44
	v_sub_f32_e32 v44, v46, v44
	v_add_f32_e32 v46, v45, v51
	v_sub_f32_e32 v45, v45, v51
	v_add_f32_e32 v51, v50, v48
	v_sub_f32_e32 v48, v50, v48
	v_add_f32_e32 v50, v49, v63
	v_sub_f32_e32 v49, v49, v63
	v_add_f32_e32 v63, v62, v60
	v_sub_f32_e32 v60, v62, v60
	v_add_f32_e32 v62, v61, v67
	v_sub_f32_e32 v61, v61, v67
	v_add_f32_e32 v67, v66, v64
	v_sub_f32_e32 v64, v66, v64
	v_add_f32_e32 v66, v65, v59
	v_sub_f32_e32 v59, v65, v59
	v_add_f32_e32 v65, v58, v56
	v_sub_f32_e32 v56, v58, v56
	v_add_f32_e32 v58, v57, v55
	v_sub_f32_e32 v55, v57, v55
	v_add_f32_e32 v57, v54, v52
	v_sub_f32_e32 v52, v54, v52
	v_add_f32_e32 v54, v53, v71
	v_sub_f32_e32 v53, v53, v71
	v_add_f32_e32 v71, v70, v68
	v_sub_f32_e32 v68, v70, v68
	v_add_f32_e32 v70, v69, v75
	v_sub_f32_e32 v69, v69, v75
	v_add_f32_e32 v75, v74, v72
	v_sub_f32_e32 v72, v74, v72
	v_add_f32_e32 v74, v73, v31
	v_sub_f32_e32 v31, v73, v31
	v_add_f32_e32 v73, v30, v28
	v_sub_f32_e32 v28, v30, v28
	v_add_f32_e32 v30, v29, v79
	v_sub_f32_e32 v29, v29, v79
	v_add_f32_e32 v79, v78, v76
	v_sub_f32_e32 v76, v78, v76
	v_add_f32_e32 v78, v77, v8
	v_sub_f32_e32 v8, v77, v8
	v_add_f32_e32 v77, v10, v9
	v_sub_f32_e32 v9, v10, v9
	v_add_f32_e32 v10, v7, v3
	v_sub_f32_e32 v3, v7, v3
	v_add_f32_e32 v7, v6, v2
	v_sub_f32_e32 v2, v6, v2
	v_add_f32_e32 v6, v4, v22
	v_sub_f32_e32 v4, v4, v22
	v_add_f32_e32 v22, v23, v35
	v_sub_f32_e32 v23, v23, v35
	v_add_f32_e32 v35, v5, v21
	v_sub_f32_e32 v5, v5, v21
	v_add_f32_e32 v21, v20, v32
	v_sub_f32_e32 v20, v20, v32
	v_add_f32_e32 v32, v34, v38
	v_sub_f32_e32 v34, v34, v38
	v_add_f32_e32 v38, v39, v43
	v_sub_f32_e32 v39, v39, v43
	v_add_f32_e32 v43, v33, v37
	v_sub_f32_e32 v33, v33, v37
	v_add_f32_e32 v37, v36, v40
	v_sub_f32_e32 v36, v36, v40
	v_add_f32_e32 v40, v42, v46
	v_sub_f32_e32 v42, v42, v46
	v_add_f32_e32 v46, v47, v51
	v_sub_f32_e32 v47, v47, v51
	v_add_f32_e32 v51, v41, v45
	v_sub_f32_e32 v41, v41, v45
	v_add_f32_e32 v45, v44, v48
	v_sub_f32_e32 v44, v44, v48
	v_add_f32_e32 v48, v50, v62
	v_sub_f32_e32 v50, v50, v62
	v_add_f32_e32 v62, v63, v67
	v_sub_f32_e32 v63, v63, v67
	v_add_f32_e32 v67, v49, v61
	v_sub_f32_e32 v49, v49, v61
	v_add_f32_e32 v61, v60, v64
	v_sub_f32_e32 v60, v60, v64
	v_add_f32_e32 v64, v66, v58
	v_sub_f32_e32 v58, v66, v58
	v_add_f32_e32 v66, v65, v57
	v_sub_f32_e32 v57, v65, v57
	v_add_f32_e32 v65, v59, v55
	v_sub_f32_e32 v55, v59, v55
	v_add_f32_e32 v59, v56, v52
	v_sub_f32_e32 v52, v56, v52
	v_add_f32_e32 v56, v54, v70
	v_sub_f32_e32 v54, v54, v70
	v_add_f32_e32 v70, v71, v75
	v_sub_f32_e32 v71, v71, v75
	v_add_f32_e32 v75, v53, v69
	v_sub_f32_e32 v53, v53, v69
	v_add_f32_e32 v69, v68, v72
	v_sub_f32_e32 v68, v68, v72
	v_add_f32_e32 v72, v74, v30
	v_sub_f32_e32 v30, v74, v30
	v_add_f32_e32 v74, v73, v79
	v_sub_f32_e32 v73, v73, v79
	v_add_f32_e32 v79, v31, v29
	v_sub_f32_e32 v29, v31, v29
	v_add_f32_e32 v31, v28, v76
	v_sub_f32_e32 v28, v28, v76
	v_add_f32_e32 v76, v78, v6
	v_sub_f32_e32 v6, v78, v6
	v_add_f32_e32 v78, v77, v22
	v_sub_f32_e32 v22, v77, v22
	v_add_f32_e32 v77, v10, v35
	v_sub_f32_e32 v10, v10, v35
	v_add_f32_e32 v35, v7, v21
	v_sub_f32_e32 v7, v7, v21
	v_add_f32_e32 v21, v8, v4
	v_sub_f32_e32 v4, v8, v4
	v_add_f32_e32 v8, v9, v23
	v_sub_f32_e32 v9, v9, v23
	v_add_f32_e32 v23, v3, v5
	v_sub_f32_e32 v3, v3, v5
	v_add_f32_e32 v5, v2, v20
	v_sub_f32_e32 v2, v2, v20
	v_add_f32_e32 v20, v32, v40
	v_sub_f32_e32 v32, v32, v40
	v_add_f32_e32 v40, v38, v46
	v_sub_f32_e32 v38, v38, v46
	v_add_f32_e32 v46, v43, v51
	v_sub_f32_e32 v43, v43, v51
	v_add_f32_e32 v51, v37, v45
	v_sub_f32_e32 v37, v37, v45
	v_add_f32_e32 v45, v34, v42
	v_sub_f32_e32 v34, v34, v42
	v_add_f32_e32 v42, v39, v47
	v_sub_f32_e32 v39, v39, v47
	v_add_f32_e32 v47, v33, v41
	v_sub_f32_e32 v33, v33, v41
	v_add_f32_e32 v41, v36, v44
	v_sub_f32_e32 v36, v36, v44
	v_add_f32_e32 v44, v48, v64
	v_sub_f32_e32 v48, v48, v64
	v_add_f32_e32 v64, v62, v66
	v_sub_f32_e32 v62, v62, v66
	v_add_f32_e32 v66, v67, v65
	v_sub_f32_e32 v65, v67, v65
	v_add_f32_e32 v67, v61, v59
	v_sub_f32_e32 v59, v61, v59
	v_add_f32_e32 v61, v50, v58
	v_sub_f32_e32 v50, v50, v58
	v_add_f32_e32 v58, v63, v57
	v_sub_f32_e32 v57, v63, v57
	v_add_f32_e32 v63, v49, v55
	v_sub_f32_e32 v49, v49, v55
	v_add_f32_e32 v55, v60, v52
	v_sub_f32_e32 v52, v60, v52
	v_add_f32_e32 v60, v56, v72
	v_sub_f32_e32 v56, v56, v72
	v_add_f32_e32 v72, v70, v74
	v_sub_f32_e32 v70, v70, v74
	v_add_f32_e32 v74, v75, v79
	v_sub_f32_e32 v75, v75, v79
	v_add_f32_e32 v79, v69, v31
	v_sub_f32_e32 v31, v69, v31
	v_add_f32_e32 v69, v54, v30
	v_sub_f32_e32 v30, v54, v30
	v_add_f32_e32 v54, v71, v73
	v_sub_f32_e32 v71, v71, v73
	v_add_f32_e32 v73, v53, v29
	v_sub_f32_e32 v29, v53, v29
	v_add_f32_e32 v53, v68, v28
	v_sub_f32_e32 v28, v68, v28
	v_add_f32_e32 v80, v78, v40
	v_sub_f32_e32 v81, v78, v40
	v_add_f32_e32 v40, v77, v46
	v_sub_f32_e32 v82, v77, v46
	v_add_f32_e32 v46, v35, v51
	v_sub_f32_e32 v51, v35, v51
	v_add_f32_e32 v35, v21, v45
	v_sub_f32_e32 v21, v21, v45
	v_add_f32_e32 v45, v8, v42
	v_sub_f32_e32 v8, v8, v42
	v_add_f32_e32 v42, v23, v47
	v_sub_f32_e32 v83, v23, v47
	v_add_f32_e32 v23, v5, v41
	v_sub_f32_e32 v100, v5, v41
	v_add_f32_e32 v103, v3, v33
	v_sub_f32_e32 v104, v3, v33
	v_add_f32_e32 v33, v2, v36
	v_sub_f32_e32 v105, v2, v36
	v_add_f32_e32 v2, v44, v60
	v_sub_f32_e32 v60, v44, v60
	v_add_f32_e32 v5, v66, v74
	v_add_f32_e32 v36, v67, v79
	v_add_f32_e32 v44, v58, v54
	v_sub_f32_e32 v54, v58, v54
	v_add_f32_e32 v58, v63, v73
	v_sub_f32_e32 v107, v63, v73
	v_add_f32_e32 v63, v55, v53
	v_add_f32_e32 v68, v76, v20
	v_add_f32_e32 v41, v6, v32
	v_sub_f32_e32 v6, v6, v32
	v_add_f32_e32 v32, v22, v38
	v_sub_f32_e32 v22, v22, v38
	v_add_f32_e32 v38, v10, v43
	v_sub_f32_e32 v101, v10, v43
	v_add_f32_e32 v10, v7, v37
	v_sub_f32_e32 v7, v7, v37
	v_add_f32_e32 v37, v4, v34
	v_sub_f32_e32 v102, v4, v34
	v_add_f32_e32 v34, v9, v39
	v_sub_f32_e32 v9, v9, v39
	v_add_f32_e32 v3, v64, v72
	v_sub_f32_e32 v106, v64, v72
	v_sub_f32_e32 v66, v66, v74
	v_sub_f32_e32 v79, v67, v79
	v_add_f32_e32 v39, v61, v69
	v_sub_f32_e32 v53, v55, v53
	v_add_f32_e32 v55, v48, v56
	v_add_f32_e32 v64, v62, v70
	v_sub_f32_e32 v108, v62, v70
	v_add_f32_e32 v62, v65, v75
	v_sub_f32_e32 v109, v65, v75
	v_add_f32_e32 v65, v59, v31
	v_sub_f32_e32 v110, v59, v31
	v_add_f32_e32 v31, v50, v30
	v_sub_f32_e32 v111, v50, v30
	v_add_f32_e32 v30, v57, v71
	v_sub_f32_e32 v112, v57, v71
	v_add_f32_e32 v57, v49, v29
	v_sub_f32_e32 v113, v49, v29
	v_add_f32_e32 v29, v52, v28
	v_add_f32_e32 v77, v40, v5
	v_sub_f32_e32 v49, v40, v5
	v_add_f32_e32 v78, v46, v36
	v_add_f32_e32 v5, v42, v58
	v_add_f32_e32 v75, v23, v63
	v_sub_f32_e32 v20, v76, v20
	v_sub_f32_e32 v61, v61, v69
	v_sub_f32_e32 v56, v48, v56
	v_add_f32_e32 v4, v68, v2
	v_sub_f32_e32 v47, v68, v2
	v_add_f32_e32 v76, v80, v3
	v_sub_f32_e32 v48, v80, v3
	v_sub_f32_e32 v50, v46, v36
	v_add_f32_e32 v2, v35, v39
	v_sub_f32_e32 v43, v35, v39
	v_add_f32_e32 v3, v45, v44
	v_sub_f32_e32 v44, v45, v44
	v_sub_f32_e32 v45, v42, v58
	v_add_f32_e32 v71, v41, v55
	v_sub_f32_e32 v39, v41, v55
	v_add_f32_e32 v73, v38, v62
	v_sub_f32_e32 v41, v38, v62
	v_add_f32_e32 v74, v10, v65
	v_sub_f32_e32 v42, v10, v65
	v_add_f32_e32 v68, v34, v30
	v_sub_f32_e32 v36, v34, v30
	v_add_f32_e32 v69, v103, v57
	v_add_f32_e32 v70, v33, v29
	v_sub_f32_e32 v38, v33, v29
	v_add_f32_e32 v65, v82, v66
	v_sub_f32_e32 v33, v82, v66
	v_add_f32_e32 v66, v51, v79
	v_sub_f32_e32 v34, v51, v79
	v_max_f32_e64 v79, |v77|, |v78|
	v_max_f32_e64 v80, |v5|, |v75|
	v_sub_f32_e32 v114, v52, v28
	v_sub_f32_e32 v46, v23, v63
	v_add_f32_e32 v72, v32, v64
	v_sub_f32_e32 v40, v32, v64
	v_add_f32_e32 v67, v37, v31
	v_add_f32_e32 v64, v81, v106
	v_sub_f32_e32 v32, v81, v106
	v_add_f32_e32 v59, v21, v61
	v_sub_f32_e32 v23, v21, v61
	v_add_f32_e32 v61, v83, v107
	v_add_f32_e32 v62, v100, v53
	v_max_f32_e64 v81, |v73|, |v74|
	v_max_f32_e64 v82, |v69|, |v70|
	v_max3_f32 v79, |v4|, |v76|, v79
	v_max3_f32 v80, |v2|, |v3|, v80
	v_sub_f32_e32 v35, v37, v31
	v_sub_f32_e32 v37, v103, v57
	v_add_f32_e32 v63, v20, v60
	v_sub_f32_e32 v31, v20, v60
	v_add_f32_e32 v60, v8, v54
	v_sub_f32_e32 v28, v8, v54
	v_sub_f32_e32 v29, v83, v107
	v_sub_f32_e32 v30, v100, v53
	v_add_f32_e32 v57, v101, v109
	v_add_f32_e32 v58, v7, v110
	v_add_f32_e32 v53, v104, v113
	v_add_f32_e32 v54, v105, v114
	v_max_f32_e64 v83, |v65|, |v66|
	v_max_f32_e64 v100, |v61|, |v62|
	v_max3_f32 v81, |v71|, |v72|, v81
	v_max3_f32 v82, |v67|, |v68|, v82
	v_max3_f32 v79, v79, 0, v80
	v_add_f32_e32 v55, v6, v56
	v_sub_f32_e32 v10, v6, v56
	v_add_f32_e32 v56, v22, v108
	v_sub_f32_e32 v21, v101, v109
	v_add_f32_e32 v51, v102, v111
	v_sub_f32_e32 v6, v102, v111
	v_add_f32_e32 v52, v9, v112
	v_max_f32_e64 v101, |v57|, |v58|
	v_max_f32_e64 v102, |v53|, |v54|
	v_max3_f32 v83, |v63|, |v64|, v83
	v_max3_f32 v100, |v59|, |v60|, v100
	v_max3_f32 v79, v79, v81, v82
	v_sub_f32_e32 v8, v104, v113
	v_max_f32_e64 v103, |v49|, |v50|
	v_max_f32_e64 v104, |v45|, |v46|
	v_max3_f32 v101, |v55|, |v56|, v101
	v_max3_f32 v102, |v51|, |v52|, v102
	v_max3_f32 v79, v79, v83, v100
	v_sub_f32_e32 v20, v22, v108
	v_sub_f32_e32 v22, v7, v110
	v_sub_f32_e32 v7, v9, v112
	v_sub_f32_e32 v9, v105, v114
	v_max_f32_e64 v105, |v41|, |v42|
	v_max_f32_e64 v106, |v37|, |v38|
	v_max3_f32 v103, |v47|, |v48|, v103
	v_max3_f32 v104, |v43|, |v44|, v104
	v_max3_f32 v79, v79, v101, v102
	v_max_f32_e64 v107, |v33|, |v34|
	v_max_f32_e64 v108, |v29|, |v30|
	v_max3_f32 v105, |v39|, |v40|, v105
	v_max3_f32 v106, |v35|, |v36|, v106
	v_max3_f32 v79, v79, v103, v104
	v_max_f32_e64 v109, |v21|, |v22|
	v_max_f32_e64 v110, |v8|, |v9|
	v_max3_f32 v107, |v31|, |v32|, v107
	v_max3_f32 v108, |v23|, |v28|, v108
	v_max3_f32 v79, v79, v105, v106
	v_max3_f32 v109, |v10|, |v20|, v109
	v_max3_f32 v110, |v6|, |v7|, v110
	v_max3_f32 v79, v79, v107, v108
	v_max3_f32 v79, v79, v109, v110
	ds_bpermute_b32 v80, v1, v79
	s_cmpk_eq_i32 s0, 0xfe
	s_cselect_b64 s[0:1], -1, 0
	s_ashr_i32 s4, s8, 7
	v_cndmask_b32_e64 v81, 0, 1, s[0:1]
	s_waitcnt lgkmcnt(0)
	v_max_f32_e32 v80, v80, v80
	v_max_f32_e32 v79, v79, v80
	ds_bpermute_b32 v80, v84, v79
	s_and_b32 s0, s4, -2
	v_cvt_pk_f16_f32 v26, v26, v27
	v_cvt_pk_f16_f32 v27, v24, v25
	s_add_i32 s0, s0, s22
	s_waitcnt lgkmcnt(0)
	v_max_f32_e32 v80, v80, v80
	v_max_f32_e32 v79, v79, v80
	ds_bpermute_b32 v80, v85, v79
	global_store_dwordx2 v[18:19], v[26:27], off offset:3080
	v_cmp_ne_u32_e64 s[4:5], 1, v81
	s_waitcnt lgkmcnt(0)
	v_max_f32_e32 v80, v80, v80
	v_max_f32_e32 v79, v79, v80
	ds_bpermute_b32 v80, v86, v79
	s_waitcnt lgkmcnt(0)
	v_max_f32_e32 v80, v80, v80
	v_max_f32_e32 v79, v79, v80
	ds_bpermute_b32 v80, v87, v79
	s_waitcnt lgkmcnt(0)
	v_max_f32_e32 v80, v80, v80
	v_max_f32_e32 v79, v79, v80
	ds_bpermute_b32 v80, v88, v79
	s_waitcnt lgkmcnt(0)
	v_max3_f32 v18, v79, v80, s33
	s_and_saveexec_b64 s[20:21], s[2:3]
	s_cbranch_execz .LBB0_1559
	s_add_u32 s38, s68, s25
	v_mul_f32_e32 v19, 0x3a810204, v18
	s_addc_u32 s39, s69, s26
	s_and_b64 vcc, exec, s[4:5]
	global_store_dword v11, v19, s[38:39]
	s_cbranch_vccnz .LBB0_1559
	s_ashr_i32 s1, s0, 31
	s_lshl_b64 s[38:39], s[0:1], 2
	s_add_u32 s38, s23, s38
	s_addc_u32 s39, s24, s39
	global_store_dword v11, v19, s[38:39]

.LBB0_1965:
	v_add_co_u32_e32 v22, vcc, s3, v16
	global_load_dwordx4 v[0:3], v[16:17], off
	global_load_dwordx4 v[4:7], v[16:17], off offset:1024
	global_load_dwordx4 v[8:11], v[16:17], off offset:2048
	global_load_dwordx4 v[12:15], v[16:17], off offset:3072
	v_addc_co_u32_e32 v23, vcc, 0, v17, vcc
	v_add_co_u32_e32 v40, vcc, s10, v16
	s_lshl_b32 s0, s2, 1
	s_nop 0
	v_addc_co_u32_e32 v41, vcc, 0, v17, vcc
	v_add_co_u32_e32 v20, vcc, s11, v16
	s_and_b32 s0, s0, 0xffffc000
	s_nop 0
	v_addc_co_u32_e32 v21, vcc, 0, v17, vcc
	global_load_dwordx4 v[24:27], v[22:23], off
	global_load_dwordx4 v[82:85], v[22:23], off offset:1024
	global_load_dwordx4 v[86:89], v[22:23], off offset:2048
	global_load_dwordx4 v[90:93], v[22:23], off offset:3072
	global_load_dwordx4 v[94:97], v[20:21], off offset:-4096
	global_load_dwordx4 v[168:171], v[40:41], off offset:1024
	global_load_dwordx4 v[172:175], v[40:41], off offset:2048
	global_load_dwordx4 v[176:179], v[40:41], off offset:3072
	global_load_dwordx4 v[180:183], v[20:21], off
	global_load_dwordx4 v[184:187], v[20:21], off offset:1024
	global_load_dwordx4 v[188:191], v[20:21], off offset:2048
	global_load_dwordx4 v[192:195], v[20:21], off offset:3072
	s_add_i32 s14, s0, 0
	v_lshl_add_u32 v22, v71, 4, s14
	ds_read_b128 v[98:101], v22
	ds_read_b128 v[102:105], v22 offset:16
	s_add_i32 s2, s2, s4
	v_lshl_add_u64 v[16:17], v[16:17], 0, s[6:7]
	s_cmpk_lt_i32 s2, 0x4000
	s_waitcnt vmcnt(15)
	v_cvt_f32_f16_sdwa v107, v0 dst_sel:DWORD dst_unused:UNUSED_PAD src0_sel:WORD_1
	v_cvt_f32_f16_sdwa v109, v1 dst_sel:DWORD dst_unused:UNUSED_PAD src0_sel:WORD_1
	v_cvt_f32_f16_sdwa v111, v2 dst_sel:DWORD dst_unused:UNUSED_PAD src0_sel:WORD_1
	v_cvt_f32_f16_sdwa v113, v3 dst_sel:DWORD dst_unused:UNUSED_PAD src0_sel:WORD_1
	v_cvt_f32_f16_e32 v106, v0
	v_cvt_f32_f16_e32 v108, v1
	v_cvt_f32_f16_e32 v110, v2
	v_cvt_f32_f16_e32 v112, v3
	s_waitcnt vmcnt(14)
	v_cvt_f32_f16_e32 v58, v4
	v_cvt_f32_f16_e32 v62, v5
	v_cvt_f32_f16_sdwa v59, v4 dst_sel:DWORD dst_unused:UNUSED_PAD src0_sel:WORD_1
	v_cvt_f32_f16_sdwa v63, v5 dst_sel:DWORD dst_unused:UNUSED_PAD src0_sel:WORD_1
	v_cvt_f32_f16_sdwa v61, v6 dst_sel:DWORD dst_unused:UNUSED_PAD src0_sel:WORD_1
	v_cvt_f32_f16_e32 v60, v6
	v_cvt_f32_f16_sdwa v65, v7 dst_sel:DWORD dst_unused:UNUSED_PAD src0_sel:WORD_1
	v_cvt_f32_f16_e32 v64, v7
	s_waitcnt vmcnt(13)
	v_cvt_f32_f16_sdwa v51, v8 dst_sel:DWORD dst_unused:UNUSED_PAD src0_sel:WORD_1
	v_cvt_f32_f16_e32 v50, v8
	v_cvt_f32_f16_sdwa v55, v9 dst_sel:DWORD dst_unused:UNUSED_PAD src0_sel:WORD_1
	v_cvt_f32_f16_e32 v54, v9
	v_cvt_f32_f16_sdwa v53, v10 dst_sel:DWORD dst_unused:UNUSED_PAD src0_sel:WORD_1
	v_cvt_f32_f16_e32 v52, v10
	v_cvt_f32_f16_sdwa v57, v11 dst_sel:DWORD dst_unused:UNUSED_PAD src0_sel:WORD_1
	v_cvt_f32_f16_e32 v56, v11
	s_waitcnt vmcnt(12)
	v_cvt_f32_f16_sdwa v43, v12 dst_sel:DWORD dst_unused:UNUSED_PAD src0_sel:WORD_1
	v_cvt_f32_f16_e32 v42, v12
	v_cvt_f32_f16_sdwa v47, v13 dst_sel:DWORD dst_unused:UNUSED_PAD src0_sel:WORD_1
	v_cvt_f32_f16_e32 v46, v13
	v_cvt_f32_f16_sdwa v45, v14 dst_sel:DWORD dst_unused:UNUSED_PAD src0_sel:WORD_1
	v_cvt_f32_f16_e32 v44, v14
	v_cvt_f32_f16_sdwa v49, v15 dst_sel:DWORD dst_unused:UNUSED_PAD src0_sel:WORD_1
	v_cvt_f32_f16_e32 v48, v15
	s_waitcnt vmcnt(9)
	v_cvt_f32_f16_e32 v8, v86
	v_cvt_f32_f16_sdwa v9, v86 dst_sel:DWORD dst_unused:UNUSED_PAD src0_sel:WORD_1
	v_cvt_f32_f16_e32 v12, v87
	v_cvt_f32_f16_sdwa v13, v87 dst_sel:DWORD dst_unused:UNUSED_PAD src0_sel:WORD_1
	v_cvt_f32_f16_e32 v10, v88
	v_cvt_f32_f16_sdwa v11, v88 dst_sel:DWORD dst_unused:UNUSED_PAD src0_sel:WORD_1
	v_cvt_f32_f16_e32 v14, v89
	v_cvt_f32_f16_sdwa v15, v89 dst_sel:DWORD dst_unused:UNUSED_PAD src0_sel:WORD_1
	s_waitcnt vmcnt(8)
	v_cvt_f32_f16_e32 v2, v92
	v_cvt_f32_f16_sdwa v3, v92 dst_sel:DWORD dst_unused:UNUSED_PAD src0_sel:WORD_1
	v_cvt_f32_f16_e32 v6, v93
	v_cvt_f32_f16_sdwa v7, v93 dst_sel:DWORD dst_unused:UNUSED_PAD src0_sel:WORD_1
	s_waitcnt vmcnt(7)
	v_cvt_f32_f16_e32 v86, v96
	v_cvt_f32_f16_sdwa v87, v96 dst_sel:DWORD dst_unused:UNUSED_PAD src0_sel:WORD_1
	v_cvt_f32_f16_e32 v88, v97
	v_cvt_f32_f16_sdwa v89, v97 dst_sel:DWORD dst_unused:UNUSED_PAD src0_sel:WORD_1
	v_mov_b32_e32 v92, v107
	v_mov_b32_e32 v93, v109
	v_mov_b32_e32 v96, v111
	v_mov_b32_e32 v97, v113
	v_cvt_f32_f16_e32 v32, v24
	v_cvt_f32_f16_sdwa v33, v24 dst_sel:DWORD dst_unused:UNUSED_PAD src0_sel:WORD_1
	v_cvt_f32_f16_e32 v36, v25
	v_cvt_f32_f16_sdwa v37, v25 dst_sel:DWORD dst_unused:UNUSED_PAD src0_sel:WORD_1
	v_cvt_f32_f16_e32 v34, v26
	v_cvt_f32_f16_sdwa v35, v26 dst_sel:DWORD dst_unused:UNUSED_PAD src0_sel:WORD_1
	v_cvt_f32_f16_e32 v38, v27
	v_cvt_f32_f16_sdwa v39, v27 dst_sel:DWORD dst_unused:UNUSED_PAD src0_sel:WORD_1
	v_cvt_f32_f16_e32 v22, v82
	v_cvt_f32_f16_sdwa v23, v82 dst_sel:DWORD dst_unused:UNUSED_PAD src0_sel:WORD_1
	v_cvt_f32_f16_e32 v26, v83
	v_cvt_f32_f16_sdwa v27, v83 dst_sel:DWORD dst_unused:UNUSED_PAD src0_sel:WORD_1
	v_cvt_f32_f16_e32 v24, v84
	v_cvt_f32_f16_sdwa v25, v84 dst_sel:DWORD dst_unused:UNUSED_PAD src0_sel:WORD_1
	v_cvt_f32_f16_e32 v28, v85
	v_cvt_f32_f16_sdwa v29, v85 dst_sel:DWORD dst_unused:UNUSED_PAD src0_sel:WORD_1
	v_cvt_f32_f16_e32 v0, v90
	v_cvt_f32_f16_sdwa v1, v90 dst_sel:DWORD dst_unused:UNUSED_PAD src0_sel:WORD_1
	v_cvt_f32_f16_e32 v4, v91
	v_cvt_f32_f16_sdwa v5, v91 dst_sel:DWORD dst_unused:UNUSED_PAD src0_sel:WORD_1
	v_cvt_f32_f16_e32 v82, v94
	v_cvt_f32_f16_sdwa v83, v94 dst_sel:DWORD dst_unused:UNUSED_PAD src0_sel:WORD_1
	v_cvt_f32_f16_e32 v84, v95
	v_cvt_f32_f16_sdwa v85, v95 dst_sel:DWORD dst_unused:UNUSED_PAD src0_sel:WORD_1
	v_mov_b32_e32 v90, v106
	v_mov_b32_e32 v91, v108
	v_mov_b32_e32 v94, v110
	v_mov_b32_e32 v95, v112
	v_pk_mul_f32 v[92:93], v[92:93], v[92:93]
	v_pk_mul_f32 v[96:97], v[96:97], v[96:97]
	v_mul_f32_e32 v30, v58, v58
	v_mul_f32_e32 v114, v62, v62
	v_pk_fma_f32 v[90:91], v[90:91], v[90:91], v[92:93]
	v_pk_fma_f32 v[92:93], v[94:95], v[94:95], v[96:97]
	v_pk_mul_f32 v[116:117], v[60:61], v[60:61]
	v_pk_mul_f32 v[118:119], v[64:65], v[64:65]
	v_pk_fma_f32 v[136:137], v[58:59], v[58:59], v[30:31] op_sel_hi:[1,1,0]
	v_pk_fma_f32 v[114:115], v[62:63], v[62:63], v[114:115] op_sel_hi:[1,1,0]
	v_pk_add_f32 v[90:91], v[90:91], v[90:91] op_sel_hi:[0,1]
	v_pk_add_f32 v[92:93], v[92:93], v[92:93] op_sel_hi:[0,1]
	v_mov_b32_e32 v122, v51
	v_mov_b32_e32 v123, v55
	v_mov_b32_e32 v136, v118
	v_mov_b32_e32 v114, v119
	v_mov_b32_e32 v90, v116
	v_mov_b32_e32 v92, v117
	v_mov_b32_e32 v120, v50
	v_mov_b32_e32 v121, v54
	v_pk_mul_f32 v[122:123], v[122:123], v[122:123]
	v_pk_add_f32 v[114:115], v[136:137], v[114:115]
	v_pk_add_f32 v[90:91], v[90:91], v[92:93]
	v_mul_f32_e32 v124, v52, v52
	v_mul_f32_e32 v126, v56, v56
	v_pk_fma_f32 v[94:95], v[120:121], v[120:121], v[122:123]
	v_pk_add_f32 v[90:91], v[90:91], v[114:115]
	v_pk_mul_f32 v[128:129], v[42:43], v[42:43]
	v_pk_mul_f32 v[130:131], v[46:47], v[46:47]
	v_pk_fma_f32 v[124:125], v[52:53], v[52:53], v[124:125] op_sel_hi:[1,1,0]
	v_pk_fma_f32 v[126:127], v[56:57], v[56:57], v[126:127] op_sel_hi:[1,1,0]
	v_pk_add_f32 v[94:95], v[94:95], v[94:95] op_sel_hi:[0,1]
	v_pk_add_f32 v[90:91], v[90:91], v[90:91] op_sel_hi:[0,1]
	v_mov_b32_e32 v134, v45
	v_mov_b32_e32 v135, v49
	v_mov_b32_e32 v124, v128
	v_mov_b32_e32 v126, v129
	v_mov_b32_e32 v94, v130
	v_mov_b32_e32 v90, v131
	v_mov_b32_e32 v132, v44
	v_mov_b32_e32 v133, v48
	v_pk_mul_f32 v[134:135], v[134:135], v[134:135]
	v_pk_add_f32 v[124:125], v[124:125], v[126:127]
	v_pk_add_f32 v[90:91], v[94:95], v[90:91]
	v_mul_f32_e32 v30, v32, v32
	v_mul_f32_e32 v138, v36, v36
	v_pk_fma_f32 v[96:97], v[132:133], v[132:133], v[134:135]
	v_pk_add_f32 v[90:91], v[124:125], v[90:91]
	v_pk_mul_f32 v[140:141], v[34:35], v[34:35]
	v_pk_mul_f32 v[142:143], v[38:39], v[38:39]
	v_pk_fma_f32 v[118:119], v[32:33], v[32:33], v[30:31] op_sel_hi:[1,1,0]
	v_pk_fma_f32 v[120:121], v[36:37], v[36:37], v[138:139] op_sel_hi:[1,1,0]
	v_pk_add_f32 v[96:97], v[96:97], v[96:97] op_sel_hi:[0,1]
	v_pk_add_f32 v[90:91], v[90:91], v[90:91] op_sel_hi:[0,1]
	v_mov_b32_e32 v146, v23
	v_mov_b32_e32 v147, v27
	v_mov_b32_e32 v118, v140
	v_mov_b32_e32 v120, v141
	v_mov_b32_e32 v96, v142
	v_mov_b32_e32 v90, v143
	v_mov_b32_e32 v144, v22
	v_mov_b32_e32 v145, v26
	v_pk_mul_f32 v[122:123], v[146:147], v[146:147]
	v_pk_add_f32 v[116:117], v[118:119], v[120:121]
	v_pk_add_f32 v[90:91], v[96:97], v[90:91]
	v_mul_f32_e32 v148, v24, v24
	v_mul_f32_e32 v150, v28, v28
	v_pk_fma_f32 v[122:123], v[144:145], v[144:145], v[122:123]
	v_pk_add_f32 v[90:91], v[116:117], v[90:91]
	v_pk_mul_f32 v[152:153], v[8:9], v[8:9]
	v_pk_mul_f32 v[154:155], v[12:13], v[12:13]
	v_pk_fma_f32 v[128:129], v[24:25], v[24:25], v[148:149] op_sel_hi:[1,1,0]
	v_pk_fma_f32 v[132:133], v[28:29], v[28:29], v[150:151] op_sel_hi:[1,1,0]
	v_pk_add_f32 v[118:119], v[122:123], v[122:123] op_sel_hi:[0,1]
	v_pk_add_f32 v[90:91], v[90:91], v[90:91] op_sel_hi:[0,1]
	v_mov_b32_e32 v158, v11
	v_mov_b32_e32 v159, v15
	v_mov_b32_e32 v128, v152
	v_mov_b32_e32 v132, v153
	v_mov_b32_e32 v118, v154
	v_mov_b32_e32 v90, v155
	v_mov_b32_e32 v156, v10
	v_mov_b32_e32 v157, v14
	v_pk_mul_f32 v[134:135], v[158:159], v[158:159]
	v_pk_add_f32 v[120:121], v[128:129], v[132:133]
	v_pk_add_f32 v[90:91], v[118:119], v[90:91]
	v_mul_f32_e32 v160, v0, v0
	v_mul_f32_e32 v162, v4, v4
	v_pk_fma_f32 v[126:127], v[156:157], v[156:157], v[134:135]
	v_pk_add_f32 v[90:91], v[120:121], v[90:91]
	v_pk_mul_f32 v[164:165], v[2:3], v[2:3]
	v_pk_mul_f32 v[166:167], v[6:7], v[6:7]
	v_pk_fma_f32 v[138:139], v[0:1], v[0:1], v[160:161] op_sel_hi:[1,1,0]
	v_pk_fma_f32 v[146:147], v[4:5], v[4:5], v[162:163] op_sel_hi:[1,1,0]
	v_pk_add_f32 v[122:123], v[126:127], v[126:127] op_sel_hi:[0,1]
	v_pk_add_f32 v[90:91], v[90:91], v[90:91] op_sel_hi:[0,1]
	v_mov_b32_e32 v138, v164
	v_mov_b32_e32 v146, v165
	v_mov_b32_e32 v122, v166
	v_mov_b32_e32 v90, v167
	v_pk_add_f32 v[126:127], v[138:139], v[146:147]
	v_pk_add_f32 v[90:91], v[122:123], v[90:91]
	s_nop 0
	v_pk_add_f32 v[90:91], v[126:127], v[90:91]
	s_nop 0
	v_add_f32_e32 v30, v90, v91
	ds_bpermute_b32 v81, v31, v30
	s_waitcnt lgkmcnt(0)
	v_add_f32_e32 v30, v30, v81
	ds_bpermute_b32 v81, v66, v30
	s_waitcnt lgkmcnt(0)
	v_add_f32_e32 v30, v30, v81
	ds_bpermute_b32 v81, v67, v30
	s_waitcnt lgkmcnt(0)
	v_add_f32_e32 v30, v30, v81
	ds_bpermute_b32 v81, v68, v30
	s_waitcnt lgkmcnt(0)
	v_add_f32_e32 v30, v30, v81
	ds_bpermute_b32 v81, v69, v30
	s_waitcnt lgkmcnt(0)
	v_add_f32_e32 v30, v30, v81
	ds_bpermute_b32 v81, v70, v30
	s_waitcnt lgkmcnt(0)
	v_add_f32_e32 v30, v30, v81
	v_fmamk_f32 v30, v30, 0x39800000, v79
	v_mul_f32_e32 v81, 0x4f800000, v30
	v_cmp_gt_f32_e32 vcc, s5, v30
	s_nop 1
	v_cndmask_b32_e32 v30, v30, v81, vcc
	v_sqrt_f32_e32 v81, v30
	s_nop 0
	v_add_u32_e32 v90, -1, v81
	v_add_u32_e32 v91, 1, v81
	v_fma_f32 v92, -v90, v81, v30
	v_fma_f32 v93, -v91, v81, v30
	v_cmp_ge_f32_e64 s[0:1], 0, v92
	s_nop 1
	v_cndmask_b32_e64 v81, v81, v90, s[0:1]
	v_cmp_lt_f32_e64 s[0:1], 0, v93
	s_nop 1
	v_cndmask_b32_e64 v81, v81, v91, s[0:1]
	v_mul_f32_e32 v90, 0x37800000, v81
	v_cndmask_b32_e32 v81, v81, v90, vcc
	v_cmp_class_f32_e32 vcc, v30, v80
	s_nop 1
	v_cndmask_b32_e32 v30, v81, v30, vcc
	v_div_scale_f32 v81, s[0:1], v30, v30, 1.0
	v_rcp_f32_e32 v91, v81
	v_div_scale_f32 v90, vcc, 1.0, v30, 1.0
	v_fma_f32 v92, -v81, v91, 1.0
	v_fmac_f32_e32 v91, v92, v91
	v_mul_f32_e32 v92, v90, v91
	v_fma_f32 v93, -v81, v92, v90
	v_fmac_f32_e32 v92, v93, v91
	v_fma_f32 v81, -v81, v92, v90
	v_div_fmas_f32 v81, v81, v91, v92
	v_div_fixup_f32 v30, v81, v30, 1.0
	v_pk_mul_f32 v[90:91], v[106:107], v[30:31] op_sel_hi:[1,0]
	v_pk_mul_f32 v[92:93], v[108:109], v[30:31] op_sel_hi:[1,0]
	v_pk_mul_f32 v[94:95], v[110:111], v[30:31] op_sel_hi:[1,0]
	v_pk_mul_f32 v[96:97], v[112:113], v[30:31] op_sel_hi:[1,0]
	v_pk_fma_f32 v[84:85], v[100:101], v[92:93], v[84:85]
	v_pk_fma_f32 v[82:83], v[98:99], v[90:91], v[82:83]
	v_pk_fma_f32 v[88:89], v[104:105], v[96:97], v[88:89]
	v_pk_fma_f32 v[86:87], v[102:103], v[94:95], v[86:87]
	global_store_dwordx4 v[18:19], v[82:85], off
	global_store_dwordx4 v[18:19], v[86:89], off offset:16
	s_nop 0
	v_lshl_add_u32 v81, v72, 4, s14
	ds_read_b128 v[86:89], v81
	ds_read_b128 v[90:93], v81 offset:16
	v_pk_mul_f32 v[94:95], v[60:61], v[30:31] op_sel_hi:[1,0]
	v_pk_mul_f32 v[58:59], v[58:59], v[30:31] op_sel_hi:[1,0]
	v_pk_mul_f32 v[62:63], v[62:63], v[30:31] op_sel_hi:[1,0]
	v_pk_mul_f32 v[64:65], v[64:65], v[30:31] op_sel_hi:[1,0]
	v_lshl_add_u32 v81, v73, 4, s14
	v_pk_mul_f32 v[50:51], v[50:51], v[30:31] op_sel_hi:[1,0]
	v_pk_mul_f32 v[54:55], v[54:55], v[30:31] op_sel_hi:[1,0]
	v_pk_mul_f32 v[56:57], v[56:57], v[30:31] op_sel_hi:[1,0]
	v_pk_mul_f32 v[44:45], v[44:45], v[30:31] op_sel_hi:[1,0]
	v_pk_mul_f32 v[32:33], v[32:33], v[30:31] op_sel_hi:[1,0]
	v_pk_mul_f32 v[36:37], v[36:37], v[30:31] op_sel_hi:[1,0]
	v_pk_mul_f32 v[38:39], v[38:39], v[30:31] op_sel_hi:[1,0]
	v_pk_mul_f32 v[22:23], v[22:23], v[30:31] op_sel_hi:[1,0]
	v_pk_mul_f32 v[26:27], v[26:27], v[30:31] op_sel_hi:[1,0]
	v_pk_mul_f32 v[28:29], v[28:29], v[30:31] op_sel_hi:[1,0]
	v_pk_mul_f32 v[8:9], v[8:9], v[30:31] op_sel_hi:[1,0]
	v_pk_mul_f32 v[12:13], v[12:13], v[30:31] op_sel_hi:[1,0]
	v_pk_mul_f32 v[14:15], v[14:15], v[30:31] op_sel_hi:[1,0]
	v_pk_mul_f32 v[0:1], v[0:1], v[30:31] op_sel_hi:[1,0]
	v_pk_mul_f32 v[4:5], v[4:5], v[30:31] op_sel_hi:[1,0]
	v_pk_mul_f32 v[6:7], v[6:7], v[30:31] op_sel_hi:[1,0]
	s_waitcnt vmcnt(8)
	v_cvt_f32_f16_e32 v96, v168
	v_cvt_f32_f16_sdwa v97, v168 dst_sel:DWORD dst_unused:UNUSED_PAD src0_sel:WORD_1
	v_cvt_f32_f16_e32 v60, v169
	v_cvt_f32_f16_sdwa v61, v169 dst_sel:DWORD dst_unused:UNUSED_PAD src0_sel:WORD_1
	v_cvt_f32_f16_e32 v82, v170
	v_cvt_f32_f16_sdwa v83, v170 dst_sel:DWORD dst_unused:UNUSED_PAD src0_sel:WORD_1
	v_cvt_f32_f16_e32 v84, v171
	v_cvt_f32_f16_sdwa v85, v171 dst_sel:DWORD dst_unused:UNUSED_PAD src0_sel:WORD_1
	s_waitcnt lgkmcnt(1)
	v_pk_fma_f32 v[60:61], v[88:89], v[62:63], v[60:61]
	v_pk_fma_f32 v[58:59], v[86:87], v[58:59], v[96:97]
	s_waitcnt lgkmcnt(0)
	v_pk_fma_f32 v[62:63], v[90:91], v[94:95], v[82:83]
	v_pk_fma_f32 v[64:65], v[92:93], v[64:65], v[84:85]
	global_store_dwordx4 v[18:19], v[58:61], off offset:2048
	global_store_dwordx4 v[18:19], v[62:65], off offset:2064
	s_nop 0
	ds_read_b128 v[62:65], v81
	ds_read_b128 v[82:85], v81 offset:16
	v_pk_mul_f32 v[90:91], v[52:53], v[30:31] op_sel_hi:[1,0]
	v_add_co_u32_e32 v86, vcc, s3, v18
	s_waitcnt vmcnt(9)
	v_cvt_f32_f16_e32 v92, v172
	v_cvt_f32_f16_sdwa v93, v172 dst_sel:DWORD dst_unused:UNUSED_PAD src0_sel:WORD_1
	v_cvt_f32_f16_e32 v52, v173
	v_cvt_f32_f16_sdwa v53, v173 dst_sel:DWORD dst_unused:UNUSED_PAD src0_sel:WORD_1
	v_cvt_f32_f16_e32 v58, v174
	v_cvt_f32_f16_sdwa v59, v174 dst_sel:DWORD dst_unused:UNUSED_PAD src0_sel:WORD_1
	v_cvt_f32_f16_e32 v60, v175
	v_cvt_f32_f16_sdwa v61, v175 dst_sel:DWORD dst_unused:UNUSED_PAD src0_sel:WORD_1
	v_addc_co_u32_e32 v87, vcc, 0, v19, vcc
	v_add_co_u32_e32 v88, vcc, s12, v18
	s_waitcnt lgkmcnt(1)
	v_pk_fma_f32 v[52:53], v[64:65], v[54:55], v[52:53]
	v_addc_co_u32_e32 v89, vcc, 0, v19, vcc
	v_pk_fma_f32 v[50:51], v[62:63], v[50:51], v[92:93]
	s_waitcnt lgkmcnt(0)
	v_pk_fma_f32 v[54:55], v[82:83], v[90:91], v[58:59]
	v_pk_fma_f32 v[56:57], v[84:85], v[56:57], v[60:61]
	global_store_dwordx4 v[88:89], v[50:53], off offset:-4096
	global_store_dwordx4 v[86:87], v[54:57], off offset:16
	s_nop 0
	v_lshl_add_u32 v40, v74, 4, s14
	ds_read_b128 v[54:57], v40
	ds_read_b128 v[58:61], v40 offset:16
	v_pk_mul_f32 v[40:41], v[42:43], v[30:31] op_sel_hi:[1,0]
	v_pk_mul_f32 v[42:43], v[46:47], v[30:31] op_sel_hi:[1,0]
	v_pk_mul_f32 v[46:47], v[48:49], v[30:31] op_sel_hi:[1,0]
	s_waitcnt vmcnt(10)
	v_cvt_f32_f16_e32 v48, v176
	v_cvt_f32_f16_sdwa v49, v176 dst_sel:DWORD dst_unused:UNUSED_PAD src0_sel:WORD_1
	v_cvt_f32_f16_e32 v50, v177
	v_cvt_f32_f16_sdwa v51, v177 dst_sel:DWORD dst_unused:UNUSED_PAD src0_sel:WORD_1
	v_cvt_f32_f16_e32 v62, v178
	v_cvt_f32_f16_sdwa v63, v178 dst_sel:DWORD dst_unused:UNUSED_PAD src0_sel:WORD_1
	v_cvt_f32_f16_e32 v52, v179
	v_cvt_f32_f16_sdwa v53, v179 dst_sel:DWORD dst_unused:UNUSED_PAD src0_sel:WORD_1
	s_waitcnt lgkmcnt(1)
	v_pk_fma_f32 v[42:43], v[56:57], v[42:43], v[50:51]
	v_pk_fma_f32 v[40:41], v[54:55], v[40:41], v[48:49]
	s_waitcnt lgkmcnt(0)
	v_pk_fma_f32 v[44:45], v[58:59], v[44:45], v[62:63]
	v_pk_fma_f32 v[46:47], v[60:61], v[46:47], v[52:53]
	global_store_dwordx4 v[86:87], v[40:43], off offset:2048
	global_store_dwordx4 v[86:87], v[44:47], off offset:2064
	s_nop 0
	v_lshl_add_u32 v48, v75, 4, s14
	ds_read_b128 v[44:47], v48
	ds_read_b128 v[48:51], v48 offset:16
	v_pk_mul_f32 v[52:53], v[34:35], v[30:31] op_sel_hi:[1,0]
	s_waitcnt vmcnt(11)
	v_cvt_f32_f16_e32 v54, v180
	v_cvt_f32_f16_sdwa v55, v180 dst_sel:DWORD dst_unused:UNUSED_PAD src0_sel:WORD_1
	v_cvt_f32_f16_e32 v34, v181
	v_cvt_f32_f16_sdwa v35, v181 dst_sel:DWORD dst_unused:UNUSED_PAD src0_sel:WORD_1
	v_cvt_f32_f16_e32 v40, v182
	v_cvt_f32_f16_sdwa v41, v182 dst_sel:DWORD dst_unused:UNUSED_PAD src0_sel:WORD_1
	v_cvt_f32_f16_e32 v42, v183
	v_cvt_f32_f16_sdwa v43, v183 dst_sel:DWORD dst_unused:UNUSED_PAD src0_sel:WORD_1
	s_waitcnt lgkmcnt(1)
	v_pk_fma_f32 v[34:35], v[36:37], v[46:47], v[34:35]
	v_pk_fma_f32 v[32:33], v[32:33], v[44:45], v[54:55]
	s_waitcnt lgkmcnt(0)
	v_pk_fma_f32 v[36:37], v[52:53], v[48:49], v[40:41]
	v_pk_fma_f32 v[38:39], v[38:39], v[50:51], v[42:43]
	global_store_dwordx4 v[88:89], v[32:35], off
	global_store_dwordx4 v[88:89], v[36:39], off offset:16
	s_nop 0
	v_lshl_add_u32 v40, v76, 4, s14
	ds_read_b128 v[36:39], v40
	ds_read_b128 v[40:43], v40 offset:16
	v_pk_mul_f32 v[44:45], v[24:25], v[30:31] op_sel_hi:[1,0]
	s_waitcnt vmcnt(12)
	v_cvt_f32_f16_e32 v46, v184
	v_cvt_f32_f16_sdwa v47, v184 dst_sel:DWORD dst_unused:UNUSED_PAD src0_sel:WORD_1
	v_cvt_f32_f16_e32 v24, v185
	v_cvt_f32_f16_sdwa v25, v185 dst_sel:DWORD dst_unused:UNUSED_PAD src0_sel:WORD_1
	v_cvt_f32_f16_e32 v32, v186
	v_cvt_f32_f16_sdwa v33, v186 dst_sel:DWORD dst_unused:UNUSED_PAD src0_sel:WORD_1
	v_cvt_f32_f16_e32 v34, v187
	v_cvt_f32_f16_sdwa v35, v187 dst_sel:DWORD dst_unused:UNUSED_PAD src0_sel:WORD_1
	s_waitcnt lgkmcnt(1)
	v_pk_fma_f32 v[24:25], v[26:27], v[38:39], v[24:25]
	v_pk_fma_f32 v[22:23], v[22:23], v[36:37], v[46:47]
	s_waitcnt lgkmcnt(0)
	v_pk_fma_f32 v[26:27], v[44:45], v[40:41], v[32:33]
	v_pk_fma_f32 v[28:29], v[28:29], v[42:43], v[34:35]
	global_store_dwordx4 v[88:89], v[22:25], off offset:2048
	global_store_dwordx4 v[88:89], v[26:29], off offset:2064
	s_nop 0
	v_lshl_add_u32 v32, v77, 4, s14
	ds_read_b128 v[26:29], v32
	ds_read_b128 v[32:35], v32 offset:16
	v_pk_mul_f32 v[38:39], v[10:11], v[30:31] op_sel_hi:[1,0]
	v_add_co_u32_e32 v36, vcc, s13, v18
	s_waitcnt vmcnt(13)
	v_cvt_f32_f16_e32 v40, v188
	v_cvt_f32_f16_sdwa v41, v188 dst_sel:DWORD dst_unused:UNUSED_PAD src0_sel:WORD_1
	v_cvt_f32_f16_e32 v10, v189
	v_cvt_f32_f16_sdwa v11, v189 dst_sel:DWORD dst_unused:UNUSED_PAD src0_sel:WORD_1
	v_cvt_f32_f16_e32 v22, v190
	v_cvt_f32_f16_sdwa v23, v190 dst_sel:DWORD dst_unused:UNUSED_PAD src0_sel:WORD_1
	v_cvt_f32_f16_e32 v24, v191
	v_cvt_f32_f16_sdwa v25, v191 dst_sel:DWORD dst_unused:UNUSED_PAD src0_sel:WORD_1
	v_addc_co_u32_e32 v37, vcc, 0, v19, vcc
	s_waitcnt lgkmcnt(1)
	v_pk_fma_f32 v[10:11], v[12:13], v[28:29], v[10:11]
	v_pk_fma_f32 v[8:9], v[8:9], v[26:27], v[40:41]
	s_waitcnt lgkmcnt(0)
	v_pk_fma_f32 v[12:13], v[38:39], v[32:33], v[22:23]
	v_pk_fma_f32 v[14:15], v[14:15], v[34:35], v[24:25]
	global_store_dwordx4 v[36:37], v[8:11], off
	global_store_dwordx4 v[36:37], v[12:15], off offset:16
	s_nop 0
	v_lshl_add_u32 v20, v78, 4, s14
	ds_read_b128 v[12:15], v20
	ds_read_b128 v[20:23], v20 offset:16
	v_pk_mul_f32 v[24:25], v[2:3], v[30:31] op_sel_hi:[1,0]
	v_lshl_add_u64 v[18:19], v[18:19], 0, s[8:9]
	s_waitcnt vmcnt(14)
	v_cvt_f32_f16_e32 v26, v192
	v_cvt_f32_f16_sdwa v27, v192 dst_sel:DWORD dst_unused:UNUSED_PAD src0_sel:WORD_1
	v_cvt_f32_f16_e32 v2, v193
	v_cvt_f32_f16_sdwa v3, v193 dst_sel:DWORD dst_unused:UNUSED_PAD src0_sel:WORD_1
	v_cvt_f32_f16_e32 v8, v194
	v_cvt_f32_f16_sdwa v9, v194 dst_sel:DWORD dst_unused:UNUSED_PAD src0_sel:WORD_1
	v_cvt_f32_f16_e32 v10, v195
	v_cvt_f32_f16_sdwa v11, v195 dst_sel:DWORD dst_unused:UNUSED_PAD src0_sel:WORD_1
	s_waitcnt lgkmcnt(1)
	v_pk_fma_f32 v[2:3], v[4:5], v[14:15], v[2:3]
	v_pk_fma_f32 v[0:1], v[0:1], v[12:13], v[26:27]
	s_waitcnt lgkmcnt(0)
	v_pk_fma_f32 v[4:5], v[24:25], v[20:21], v[8:9]
	v_pk_fma_f32 v[6:7], v[6:7], v[22:23], v[10:11]
	global_store_dwordx4 v[36:37], v[0:3], off offset:2048
	global_store_dwordx4 v[36:37], v[4:7], off offset:2064
	s_cbranch_scc1 .LBB0_1965
